# v25: v23 + ffn_norm_route hot loop: table loads of 4 column blocks issued together into the (moved) prefetch registers, prefetch issued after the table section, explicit drain before bottom copies
# speedup vs baseline: 1.0174x; 1.0062x over previous
.LBB0_1736:
	s_or_b64 exec, exec, s[28:29]
	s_waitcnt vmcnt(0)
	s_add_i32 s34, s34, 2
	s_add_i32 s18, s18, s38
	s_cmp_eq_u32 s39, s56
	v_mov_b32_e32 v134, v217
	v_mov_b32_e32 v135, v216
	v_mov_b32_e32 v148, v215
	v_mov_b32_e32 v149, v214
	v_mov_b32_e32 v150, v213
	v_mov_b32_e32 v146, v212
	v_mov_b32_e32 v173, v218
	v_mov_b32_e32 v171, v219
	v_mov_b32_e32 v170, v220
	v_mov_b32_e32 v172, v221
	v_mov_b32_e32 v169, v222
	v_mov_b32_e32 v168, v223
	v_mov_b32_e32 v166, v224
	v_mov_b32_e32 v160, v225
	v_mov_b32_e32 v155, v226
	v_mov_b32_e32 v154, v227
	v_mov_b64_e32 v[130:131], v[96:97]
	v_mov_b64_e32 v[94:95], v[98:99]
	v_mov_b64_e32 v[84:85], v[100:101]
	v_mov_b64_e32 v[92:93], v[102:103]
	v_mov_b64_e32 v[80:81], v[104:105]
	v_mov_b64_e32 v[82:83], v[106:107]
	v_mov_b64_e32 v[86:87], v[108:109]
	v_mov_b64_e32 v[144:145], v[110:111]
	v_mov_b64_e32 v[142:143], v[112:113]
	v_mov_b64_e32 v[140:141], v[114:115]
	v_mov_b64_e32 v[128:129], v[116:117]
	v_mov_b64_e32 v[138:139], v[118:119]
	v_mov_b64_e32 v[88:89], v[120:121]
	v_mov_b64_e32 v[90:91], v[122:123]
	v_mov_b64_e32 v[132:133], v[124:125]
	v_mov_b64_e32 v[136:137], v[126:127]
	s_cbranch_scc1 .LBB0_1858

.LBB0_1739:
	s_andn2_b64 vcc, exec, s[6:7]
	s_waitcnt vmcnt(9)
	v_mov_b32_e32 v217, v134
	s_waitcnt vmcnt(8)
	v_mov_b32_e32 v216, v135
	s_waitcnt vmcnt(7)
	v_mov_b32_e32 v215, v148
	s_waitcnt vmcnt(6)
	v_mov_b32_e32 v214, v149
	s_waitcnt vmcnt(5)
	v_mov_b32_e32 v213, v150
	s_waitcnt vmcnt(4)
	v_mov_b32_e32 v212, v146
	v_mov_b32_e32 v218, v173
	v_mov_b32_e32 v219, v171
	v_mov_b32_e32 v220, v170
	v_mov_b32_e32 v221, v172
	v_mov_b32_e32 v222, v169
	v_mov_b32_e32 v223, v168
	v_mov_b32_e32 v224, v166
	v_mov_b32_e32 v225, v160
	v_mov_b32_e32 v226, v155
	v_mov_b32_e32 v227, v154
	s_waitcnt vmcnt(0)
	v_mov_b64_e32 v[96:97], v[130:131]
	v_mov_b64_e32 v[98:99], v[94:95]
	v_mov_b64_e32 v[100:101], v[84:85]
	v_mov_b64_e32 v[102:103], v[92:93]
	v_mov_b64_e32 v[104:105], v[80:81]
	v_mov_b64_e32 v[106:107], v[82:83]
	v_mov_b64_e32 v[108:109], v[86:87]
	v_mov_b64_e32 v[110:111], v[144:145]
	v_mov_b64_e32 v[112:113], v[142:143]
	v_mov_b64_e32 v[114:115], v[140:141]
	v_mov_b64_e32 v[116:117], v[128:129]
	v_mov_b64_e32 v[118:119], v[138:139]
	v_mov_b64_e32 v[120:121], v[88:89]
	v_mov_b64_e32 v[122:123], v[90:91]
	v_mov_b64_e32 v[124:125], v[132:133]
	v_mov_b64_e32 v[126:127], v[136:137]
	v_ashrrev_i32_e32 v77, 31, v76
	v_ashrrev_i32_e32 v75, 31, v74
	v_ashrrev_i32_e32 v73, 31, v72
	v_ashrrev_i32_e32 v71, 31, v70
	v_ashrrev_i32_e32 v69, 31, v68
	v_ashrrev_i32_e32 v67, 31, v66
	v_ashrrev_i32_e32 v65, 31, v64
.LBB0_1741:
	v_cvt_pk_f32_fp8_e32 v[152:153], v146
	v_cvt_pk_f32_fp8_sdwa v[156:157], v146 src0_sel:WORD_1
	v_lshlrev_b32_e32 v146, 16, v130
	v_and_b32_e32 v147, 0xffff0000, v130
	v_lshlrev_b32_e32 v130, 16, v131
	v_and_b32_e32 v131, 0xffff0000, v131
	v_pk_add_f32 v[146:147], v[152:153], v[146:147]
	v_pk_add_f32 v[152:153], v[156:157], v[130:131]
	v_cvt_pk_f32_fp8_e32 v[130:131], v150
	v_cvt_pk_f32_fp8_sdwa v[150:151], v150 src0_sel:WORD_1
	v_lshlrev_b32_e32 v156, 16, v94
	v_and_b32_e32 v157, 0xffff0000, v94
	v_lshlrev_b32_e32 v94, 16, v95
	v_and_b32_e32 v95, 0xffff0000, v95
	v_pk_add_f32 v[164:165], v[150:151], v[94:95]
	v_cvt_pk_f32_fp8_e32 v[94:95], v149
	v_cvt_pk_f32_fp8_e32 v[150:151], v148
	v_pk_add_f32 v[162:163], v[130:131], v[156:157]
	v_cvt_pk_f32_fp8_sdwa v[130:131], v149 src0_sel:WORD_1
	v_cvt_pk_f32_fp8_sdwa v[158:159], v148 src0_sel:WORD_1
	v_lshlrev_b32_e32 v149, 16, v92
	v_lshlrev_b32_e32 v148, 16, v84
	v_mov_b32_e32 v156, v94
	v_mov_b32_e32 v157, v150
	v_pk_add_f32 v[148:149], v[156:157], v[148:149]
	v_and_b32_e32 v157, 0xffff0000, v92
	v_and_b32_e32 v156, 0xffff0000, v84
	v_mov_b32_e32 v150, v95
	v_pk_add_f32 v[150:151], v[150:151], v[156:157]
	v_lshlrev_b32_e32 v95, 16, v93
	v_lshlrev_b32_e32 v94, 16, v85
	v_mov_b32_e32 v156, v130
	v_mov_b32_e32 v157, v158
	v_pk_add_f32 v[156:157], v[156:157], v[94:95]
	v_and_b32_e32 v92, 0xffff0000, v85
	v_cvt_pk_f32_fp8_e32 v[84:85], v135
	v_cvt_pk_f32_fp8_e32 v[94:95], v134
	v_cvt_pk_f32_fp8_sdwa v[174:175], v135 src0_sel:WORD_1
	v_cvt_pk_f32_fp8_sdwa v[134:135], v134 src0_sel:WORD_1
	v_and_b32_e32 v93, 0xffff0000, v93
	v_mov_b32_e32 v158, v131
	v_pk_add_f32 v[158:159], v[158:159], v[92:93]
	v_lshlrev_b32_e32 v93, 16, v82
	v_lshlrev_b32_e32 v92, 16, v80
	v_mov_b32_e32 v130, v84
	v_mov_b32_e32 v131, v94
	v_pk_add_f32 v[92:93], v[130:131], v[92:93]
	v_and_b32_e32 v131, 0xffff0000, v82
	v_and_b32_e32 v130, 0xffff0000, v80
	v_mov_b32_e32 v94, v85
	v_pk_add_f32 v[94:95], v[94:95], v[130:131]
	v_lshlrev_b32_e32 v85, 16, v83
	v_lshlrev_b32_e32 v84, 16, v81
	v_mov_b32_e32 v130, v174
	v_mov_b32_e32 v131, v134
	v_and_b32_e32 v83, 0xffff0000, v83
	v_and_b32_e32 v82, 0xffff0000, v81
	v_mov_b32_e32 v134, v175
	v_pk_add_f32 v[130:131], v[130:131], v[84:85]
	v_pk_add_f32 v[134:135], v[134:135], v[82:83]
	v_cvt_pk_f32_fp8_e32 v[82:83], v173
	v_cvt_pk_f32_fp8_e32 v[84:85], v171
	v_cvt_pk_f32_fp8_sdwa v[174:175], v173 src0_sel:WORD_1
	v_cvt_pk_f32_fp8_sdwa v[176:177], v171 src0_sel:WORD_1
	v_lshlrev_b32_e32 v81, 16, v144
	v_lshlrev_b32_e32 v80, 16, v86
	v_mov_b32_e32 v178, v82
	v_mov_b32_e32 v179, v84
	v_pk_add_f32 v[80:81], v[178:179], v[80:81]
	v_and_b32_e32 v179, 0xffff0000, v144
	v_and_b32_e32 v178, 0xffff0000, v86
	v_mov_b32_e32 v84, v83
	v_pk_add_f32 v[82:83], v[84:85], v[178:179]
	v_lshlrev_b32_e32 v85, 16, v145
	v_mov_b32_e32 v179, v176
	v_and_b32_e32 v145, 0xffff0000, v145
	v_and_b32_e32 v144, 0xffff0000, v87
	v_mov_b32_e32 v176, v175
	v_lshlrev_b32_e32 v84, 16, v87
	v_pk_add_f32 v[86:87], v[176:177], v[144:145]
	v_cvt_pk_f32_fp8_e32 v[144:145], v170
	v_mov_b32_e32 v178, v174
	v_cvt_pk_f32_fp8_sdwa v[174:175], v170 src0_sel:WORD_1
	v_lshlrev_b32_e32 v170, 16, v142
	v_and_b32_e32 v171, 0xffff0000, v142
	v_pk_add_f32 v[170:171], v[144:145], v[170:171]
	v_cvt_pk_f32_fp8_sdwa v[144:145], v172 src0_sel:WORD_1
	v_lshlrev_b32_e32 v142, 16, v143
	v_and_b32_e32 v143, 0xffff0000, v143
	v_pk_add_f32 v[174:175], v[174:175], v[142:143]
	v_cvt_pk_f32_fp8_e32 v[142:143], v172
	v_lshlrev_b32_e32 v172, 16, v140
	v_and_b32_e32 v173, 0xffff0000, v140
	v_lshlrev_b32_e32 v140, 16, v141
	v_and_b32_e32 v141, 0xffff0000, v141
	v_pk_add_f32 v[182:183], v[144:145], v[140:141]
	v_cvt_pk_f32_fp8_e32 v[140:141], v169
	v_cvt_pk_f32_fp8_e32 v[144:145], v168
	v_pk_add_f32 v[84:85], v[178:179], v[84:85]
	v_pk_add_f32 v[180:181], v[142:143], v[172:173]
	v_cvt_pk_f32_fp8_sdwa v[142:143], v169 src0_sel:WORD_1
	v_cvt_pk_f32_fp8_sdwa v[178:179], v168 src0_sel:WORD_1
	v_lshlrev_b32_e32 v169, 16, v138
	v_lshlrev_b32_e32 v168, 16, v128
	v_mov_b32_e32 v172, v140
	v_mov_b32_e32 v173, v144
	v_pk_add_f32 v[168:169], v[172:173], v[168:169]
	v_and_b32_e32 v173, 0xffff0000, v138
	v_and_b32_e32 v172, 0xffff0000, v128
	v_mov_b32_e32 v144, v141
	v_pk_add_f32 v[172:173], v[144:145], v[172:173]
	v_lshlrev_b32_e32 v141, 16, v139
	v_lshlrev_b32_e32 v140, 16, v129
	v_mov_b32_e32 v144, v142
	v_mov_b32_e32 v145, v178
	v_pk_add_f32 v[176:177], v[144:145], v[140:141]
	v_and_b32_e32 v138, 0xffff0000, v129
	v_cvt_pk_f32_fp8_e32 v[128:129], v166
	v_cvt_pk_f32_fp8_e32 v[140:141], v160
	v_cvt_pk_f32_fp8_sdwa v[144:145], v166 src0_sel:WORD_1
	v_cvt_pk_f32_fp8_sdwa v[184:185], v160 src0_sel:WORD_1
	v_and_b32_e32 v139, 0xffff0000, v139
	v_mov_b32_e32 v178, v143
	v_pk_add_f32 v[178:179], v[178:179], v[138:139]
	v_lshlrev_b32_e32 v139, 16, v90
	v_lshlrev_b32_e32 v138, 16, v88
	v_mov_b32_e32 v142, v128
	v_mov_b32_e32 v143, v140
	v_pk_add_f32 v[138:139], v[142:143], v[138:139]
	v_and_b32_e32 v143, 0xffff0000, v90
	v_and_b32_e32 v142, 0xffff0000, v88
	v_mov_b32_e32 v140, v129
	v_pk_add_f32 v[140:141], v[140:141], v[142:143]
	v_lshlrev_b32_e32 v129, 16, v91
	v_lshlrev_b32_e32 v128, 16, v89
	v_mov_b32_e32 v142, v144
	v_mov_b32_e32 v143, v184
	v_and_b32_e32 v91, 0xffff0000, v91
	v_and_b32_e32 v90, 0xffff0000, v89
	v_mov_b32_e32 v184, v145
	v_pk_add_f32 v[142:143], v[142:143], v[128:129]
	v_pk_add_f32 v[144:145], v[184:185], v[90:91]
	v_cvt_pk_f32_fp8_e32 v[90:91], v155
	v_cvt_pk_f32_fp8_e32 v[128:129], v154
	v_lshlrev_b32_e32 v89, 16, v136
	v_lshlrev_b32_e32 v88, 16, v132
	v_mov_b32_e32 v186, v90
	v_mov_b32_e32 v187, v128
	v_pk_mul_f32 v[228:229], v[146:147], v[146:147]
	v_pk_mul_f32 v[232:233], v[162:163], v[162:163]
	v_pk_add_f32 v[88:89], v[186:187], v[88:89]
	v_and_b32_e32 v187, 0xffff0000, v136
	v_and_b32_e32 v186, 0xffff0000, v132
	v_pk_mul_f32 v[230:231], v[152:153], v[152:153]
	v_pk_mul_f32 v[234:235], v[164:165], v[164:165]
	v_pk_mul_f32 v[236:237], v[150:151], v[150:151]
	v_add_f32_e32 v132, v232, v233
	v_add_f32_e32 v136, v228, v229
	v_pk_fma_f32 v[236:237], v[148:149], v[148:149], v[236:237]
	v_add_f32_e32 v132, v234, v132
	v_add_f32_e32 v136, v230, v136
	v_pk_fma_f32 v[236:237], v[156:157], v[156:157], v[236:237]
	v_pk_mul_f32 v[238:239], v[94:95], v[94:95]
	v_add_f32_e32 v132, v235, v132
	v_add_f32_e32 v136, v231, v136
	v_pk_fma_f32 v[236:237], v[158:159], v[158:159], v[236:237]
	v_pk_fma_f32 v[238:239], v[92:93], v[92:93], v[238:239]
	v_add_f32_e32 v132, v136, v132
	v_pk_fma_f32 v[238:239], v[130:131], v[130:131], v[238:239]
	v_pk_mul_f32 v[240:241], v[82:83], v[82:83]
	v_add_f32_e32 v132, v132, v236
	v_pk_fma_f32 v[238:239], v[134:135], v[134:135], v[238:239]
	v_pk_fma_f32 v[240:241], v[80:81], v[80:81], v[240:241]
	v_add_f32_e32 v132, v132, v237
	v_pk_fma_f32 v[240:241], v[84:85], v[84:85], v[240:241]
	v_add_f32_e32 v132, v132, v238
	v_pk_fma_f32 v[240:241], v[86:87], v[86:87], v[240:241]
	v_add_f32_e32 v132, v132, v239
	v_add_f32_e32 v132, v132, v240
	v_add_f32_e32 v132, v132, v241
	v_cvt_pk_f32_fp8_sdwa v[184:185], v155 src0_sel:WORD_1
	v_cvt_pk_f32_fp8_sdwa v[154:155], v154 src0_sel:WORD_1
	v_add_f32_dpp v132, v132, v132 quad_perm:[1,0,3,2] row_mask:0xf bank_mask:0xf bound_ctrl:1
	v_mov_b32_e32 v128, v91
	v_pk_add_f32 v[90:91], v[128:129], v[186:187]
	v_add_f32_dpp v132, v132, v132 quad_perm:[2,3,0,1] row_mask:0xf bank_mask:0xf bound_ctrl:1
	v_mov_b32_e32 v187, v154
	v_mov_b32_e32 v186, v184
	v_add_f32_dpp v132, v132, v132 row_half_mirror row_mask:0xf bank_mask:0xf bound_ctrl:1
	v_lshlrev_b64 v[234:235], 2, v[78:79]
	v_lshlrev_b32_e32 v129, 16, v137
	v_add_f32_dpp v132, v132, v132 row_mirror row_mask:0xf bank_mask:0xf bound_ctrl:1
	v_lshlrev_b32_e32 v128, 16, v133
	v_readlane_b32 s8, v132, 16
	v_readlane_b32 s9, v132, 48
	v_readlane_b32 s6, v132, 0
	v_readlane_b32 s7, v132, 32
	v_mov_b32_e32 v228, s8
	v_mov_b32_e32 v229, s9
	v_pk_add_f32 v[228:229], s[6:7], v[228:229]
	v_pk_add_f32 v[128:129], v[186:187], v[128:129]
	v_add_f32_e32 v132, v228, v229
	v_fmamk_f32 v132, v132, 0x3a000000, v206
	v_mul_f32_e32 v136, 0x4f800000, v132
	v_cmp_gt_f32_e32 vcc, s49, v132
	v_and_b32_e32 v137, 0xffff0000, v137
	v_pk_mul_f32 v[228:229], v[180:181], v[180:181]
	v_cndmask_b32_e32 v132, v132, v136, vcc
	v_sqrt_f32_e32 v136, v132
	v_pk_mul_f32 v[238:239], v[182:183], v[182:183]
	v_add_f32_e32 v228, v228, v229
	v_add_f32_e32 v228, v238, v228
	v_add_u32_e32 v154, -1, v136
	v_fma_f32 v160, -v154, v136, v132
	v_cmp_ge_f32_e64 s[6:7], 0, v160
	v_add_u32_e32 v160, 1, v136
	v_pk_mul_f32 v[242:243], v[140:141], v[140:141]
	v_cndmask_b32_e64 v154, v136, v154, s[6:7]
	v_fma_f32 v136, -v160, v136, v132
	v_cmp_lt_f32_e64 s[6:7], 0, v136
	v_add_f32_e32 v228, v239, v228
	v_pk_fma_f32 v[242:243], v[138:139], v[138:139], v[242:243]
	v_cndmask_b32_e64 v136, v154, v160, s[6:7]
	v_mul_f32_e32 v154, 0x37800000, v136
	v_cndmask_b32_e32 v136, v136, v154, vcc
	v_cmp_class_f32_e32 vcc, v132, v207
	v_mov_b32_e32 v154, v185
	v_pk_mul_f32 v[184:185], v[172:173], v[172:173]
	v_cndmask_b32_e32 v160, v136, v132, vcc
	v_div_scale_f32 v166, s[6:7], v160, v160, 1.0
	s_ashr_i32 s6, s18, 12
	s_mul_hi_i32 s7, s6, 0xc000
	s_mul_i32 s6, s6, 0xc000
	s_add_u32 s6, s2, s6
	s_addc_u32 s7, s3, s7
	s_add_u32 s10, s6, 0xe000
	s_addc_u32 s11, s7, 0
	v_pk_fma_f32 v[230:231], v[168:169], v[168:169], v[184:185]
	s_add_u32 s12, s6, 0x10000
	s_addc_u32 s13, s7, 0
	v_pk_fma_f32 v[230:231], v[176:177], v[176:177], v[230:231]
	v_lshl_add_u64 v[184:185], s[12:13], 0, v[234:235]
	v_pk_fma_f32 v[240:241], v[178:179], v[178:179], v[230:231]
	s_waitcnt lgkmcnt(0)
	v_lshl_add_u64 v[230:231], s[24:25], 0, v[234:235]
	v_lshlrev_b32_e32 v250, 4, v189
	v_add_u32_e32 v251, 0x1000, v250
	global_load_dwordx4 v[96:99], v250, s[12:13]
	global_load_dwordx4 v[100:103], v250, s[24:25]
	global_load_dwordx4 v[104:107], v250, s[10:11]
	global_load_dwordx4 v[108:111], v250, s[12:13] offset:1024
	global_load_dwordx4 v[112:115], v250, s[24:25] offset:1024
	global_load_dwordx4 v[116:119], v250, s[10:11] offset:1024
	global_load_dwordx4 v[120:123], v250, s[12:13] offset:2048
	global_load_dwordx4 v[124:127], v250, s[24:25] offset:2048
	global_load_dwordx4 v[212:215], v250, s[10:11] offset:2048
	global_load_dwordx4 v[216:219], v250, s[12:13] offset:3072
	global_load_dwordx4 v[220:223], v250, s[24:25] offset:3072
	global_load_dwordx4 v[224:227], v250, s[10:11] offset:3072
	v_lshl_add_u64 v[234:235], s[10:11], 0, v[234:235]
	v_rcp_f32_e32 v246, v166
	v_and_b32_e32 v136, 0xffff0000, v133
	v_pk_add_f32 v[132:133], v[154:155], v[136:137]
	v_fma_f32 v136, -v166, v246, 1.0
	v_fmac_f32_e32 v246, v136, v246
	v_pk_mul_f32 v[136:137], v[170:171], v[170:171]
	v_pk_mul_f32 v[154:155], v[174:175], v[174:175]
	v_add_f32_e32 v136, v136, v137
	v_add_f32_e32 v136, v154, v136
	v_add_f32_e32 v136, v155, v136
	v_add_f32_e32 v136, v136, v228
	v_pk_fma_f32 v[242:243], v[142:143], v[142:143], v[242:243]
	v_pk_mul_f32 v[244:245], v[90:91], v[90:91]
	v_add_f32_e32 v136, v136, v240
	v_pk_fma_f32 v[242:243], v[144:145], v[144:145], v[242:243]
	v_pk_fma_f32 v[244:245], v[88:89], v[88:89], v[244:245]
	v_add_f32_e32 v136, v136, v241
	v_pk_fma_f32 v[244:245], v[128:129], v[128:129], v[244:245]
	v_add_f32_e32 v136, v136, v242
	v_pk_fma_f32 v[244:245], v[132:133], v[132:133], v[244:245]
	v_add_f32_e32 v136, v136, v243
	v_add_f32_e32 v136, v136, v244
	v_add_f32_e32 v136, v136, v245
	v_div_scale_f32 v247, vcc, 1.0, v160, 1.0
	s_nop 0
	v_add_f32_dpp v136, v136, v136 quad_perm:[1,0,3,2] row_mask:0xf bank_mask:0xf bound_ctrl:1
	v_mul_f32_e32 v248, v247, v246
	v_fma_f32 v154, -v166, v248, v247
	v_add_f32_dpp v136, v136, v136 quad_perm:[2,3,0,1] row_mask:0xf bank_mask:0xf bound_ctrl:1
	v_fmac_f32_e32 v248, v154, v246
	v_fma_f32 v154, -v166, v248, v247
	v_add_f32_dpp v136, v136, v136 row_half_mirror row_mask:0xf bank_mask:0xf bound_ctrl:1
	v_div_fmas_f32 v154, v154, v246, v248
	v_lshrrev_b32_e32 v229, 1, v189
	v_add_f32_dpp v136, v136, v136 row_mirror row_mask:0xf bank_mask:0xf bound_ctrl:1
	v_add_u32_e32 v246, 64, v229
	v_readlane_b32 s8, v136, 16
	v_readlane_b32 s9, v136, 48
	v_readlane_b32 s6, v136, 0
	v_readlane_b32 s7, v136, 32
	v_mov_b32_e32 v136, s8
	v_mov_b32_e32 v137, s9
	v_pk_add_f32 v[136:137], s[6:7], v[136:137]
	s_ashr_i32 s19, s18, 31
	v_add_f32_e32 v136, v136, v137
	v_fmamk_f32 v136, v136, 0x3a000000, v206
	v_mul_f32_e32 v137, 0x4f800000, v136
	v_cmp_gt_f32_e64 s[6:7], s49, v136
	s_waitcnt vmcnt(11)
	v_pk_add_f32 v[96:97], v[96:97], 1.0 op_sel_hi:[1,0]
	v_cndmask_b32_e64 v136, v136, v137, s[6:7]
	v_sqrt_f32_e32 v137, v136
	s_nop 0
	v_add_u32_e32 v155, -1, v137
	v_fma_f32 v166, -v155, v137, v136
	v_cmp_ge_f32_e64 s[8:9], 0, v166
	v_add_u32_e32 v166, 1, v137
	s_nop 0
	v_cndmask_b32_e64 v155, v137, v155, s[8:9]
	v_fma_f32 v137, -v166, v137, v136
	v_cmp_lt_f32_e64 s[8:9], 0, v137
	s_nop 1
	v_cndmask_b32_e64 v137, v155, v166, s[8:9]
	v_mul_f32_e32 v155, 0x37800000, v137
	v_cndmask_b32_e64 v137, v137, v155, s[6:7]
	v_cmp_class_f32_e64 s[6:7], v136, v207
	v_div_fixup_f32 v166, v154, v160, 1.0
	v_pk_mul_f32 v[146:147], v[146:147], v[166:167] op_sel_hi:[1,0]
	v_cndmask_b32_e64 v136, v137, v136, s[6:7]
	v_div_scale_f32 v137, s[6:7], v136, v136, 1.0
	v_rcp_f32_e32 v155, v137
	s_waitcnt vmcnt(10)
	v_pk_mul_f32 v[146:147], v[100:101], v[146:147]
	v_pk_mul_f32 v[152:153], v[152:153], v[166:167] op_sel_hi:[1,0]
	v_pk_mul_f32 v[164:165], v[164:165], v[166:167] op_sel_hi:[1,0]
	v_fma_f32 v154, -v137, v155, 1.0
	v_fmac_f32_e32 v155, v154, v155
	v_div_scale_f32 v154, vcc, 1.0, v136, 1.0
	v_mul_f32_e32 v160, v154, v155
	v_fma_f32 v228, -v137, v160, v154
	v_fmac_f32_e32 v160, v228, v155
	v_fma_f32 v137, -v137, v160, v154
	v_div_fmas_f32 v137, v137, v155, v160
	v_div_fixup_f32 v160, v137, v136, 1.0
	v_lshlrev_b32_e32 v136, 3, v189
	v_and_b32_e32 v228, 8, v136
	v_pk_add_f32 v[136:137], v[98:99], 1.0 op_sel_hi:[1,0]
	s_waitcnt vmcnt(9)
	v_pk_fma_f32 v[154:155], v[96:97], v[146:147], v[104:105]
	v_pk_mul_f32 v[152:153], v[102:103], v[152:153]
	v_cvt_pk_bf16_f32 v146, v154, v155
	v_pk_mul_f32 v[170:171], v[170:171], v[160:161] op_sel_hi:[1,0]
	v_lshlrev_b32_e32 v186, 16, v146
	v_and_b32_e32 v187, 0xffff0000, v146
	v_sub_f32_e32 v186, v154, v186
	v_sub_f32_e32 v187, v155, v187
	v_pk_fma_f32 v[152:153], v[136:137], v[152:153], v[106:107]
	v_pk_mul_f32 v[170:171], v[100:101], v[170:171]
	v_cvt_pk_bf16_f32 v147, v152, v153
	v_cvt_pk_bf16_f32 v186, v186, v187
	v_pk_mul_f32 v[162:163], v[162:163], v[166:167] op_sel_hi:[1,0]
	v_lshlrev_b32_e32 v187, 16, v147
	v_and_b32_e32 v238, 0xffff0000, v147
	v_sub_f32_e32 v187, v152, v187
	v_sub_f32_e32 v238, v153, v238
	v_cvt_pk_bf16_f32 v187, v187, v238
	v_xor_b32_e32 v238, s43, v229
	v_lshlrev_b32_e32 v238, 4, v238
	v_add3_u32 v238, s44, v238, v228
	ds_write_b64 v238, v[146:147]
	v_add_u32_e32 v146, 0x10000, v238
	ds_write_b64 v146, v[186:187]
	v_pk_mul_f32 v[146:147], v[174:175], v[160:161] op_sel_hi:[1,0]
	v_xor_b32_e32 v238, s45, v229
	v_pk_mul_f32 v[146:147], v[102:103], v[146:147]
	v_lshlrev_b32_e32 v238, 4, v238
	v_pk_fma_f32 v[136:137], v[136:137], v[146:147], v[106:107]
	v_pk_fma_f32 v[146:147], v[96:97], v[170:171], v[104:105]
	v_lshlrev_b64 v[234:235], 2, v[76:77]
	v_cvt_pk_bf16_f32 v170, v146, v147
	v_cvt_pk_bf16_f32 v171, v136, v137
	v_lshl_add_u64 v[230:231], s[24:25], 0, v[234:235]
	v_lshlrev_b32_e32 v174, 16, v170
	v_and_b32_e32 v175, 0xffff0000, v170
	v_sub_f32_e32 v174, v146, v174
	v_sub_f32_e32 v175, v147, v175
	v_cvt_pk_bf16_f32 v174, v174, v175
	v_lshlrev_b32_e32 v175, 16, v171
	v_and_b32_e32 v184, 0xffff0000, v171
	v_sub_f32_e32 v175, v136, v175
	v_sub_f32_e32 v184, v137, v184
	v_cvt_pk_bf16_f32 v175, v175, v184
	v_lshl_add_u64 v[184:185], s[12:13], 0, v[234:235]
	v_lshl_add_u64 v[234:235], s[10:11], 0, v[234:235]
	v_add3_u32 v238, s46, v238, v228
	ds_write_b64 v238, v[170:171]
	v_add_u32_e32 v170, 0x10000, v238
	ds_write_b64 v170, v[174:175]
	v_add_u32_e32 v238, 32, v229
	s_lshl_b64 s[6:7], s[18:19], 11
	s_add_u32 s6, s41, s6
	s_addc_u32 s7, s42, s7
	s_waitcnt vmcnt(8)
	v_pk_add_f32 v[110:111], v[110:111], 1.0 op_sel_hi:[1,0]
	v_pk_add_f32 v[108:109], v[108:109], 1.0 op_sel_hi:[1,0]
	s_waitcnt vmcnt(7)
	v_pk_mul_f32 v[162:163], v[162:163], v[112:113]
	v_pk_mul_f32 v[164:165], v[164:165], v[114:115]
	s_waitcnt vmcnt(6)
	v_pk_fma_f32 v[174:175], v[162:163], v[108:109], v[116:117]
	v_pk_fma_f32 v[170:171], v[164:165], v[110:111], v[118:119]
	v_cvt_pk_bf16_f32 v162, v174, v175
	s_nop 0
	v_lshlrev_b32_e32 v164, 16, v162
	v_and_b32_e32 v165, 0xffff0000, v162
	v_sub_f32_e32 v164, v174, v164
	v_sub_f32_e32 v165, v175, v165
	v_cvt_pk_bf16_f32 v163, v170, v171
	v_cvt_pk_bf16_f32 v164, v164, v165
	s_nop 0
	v_lshlrev_b32_e32 v165, 16, v163
	v_and_b32_e32 v239, 0xffff0000, v163
	v_sub_f32_e32 v165, v170, v165
	v_sub_f32_e32 v239, v171, v239
	v_cvt_pk_bf16_f32 v165, v165, v239
	v_xor_b32_e32 v239, s43, v238
	v_lshlrev_b32_e32 v239, 4, v239
	v_add3_u32 v239, s44, v239, v228
	ds_write_b64 v239, v[162:163]
	v_add_u32_e32 v162, 0x10000, v239
	ds_write_b64 v162, v[164:165]
	v_pk_mul_f32 v[164:165], v[180:181], v[160:161] op_sel_hi:[1,0]
	v_pk_mul_f32 v[162:163], v[182:183], v[160:161] op_sel_hi:[1,0]
	v_pk_mul_f32 v[164:165], v[164:165], v[112:113]
	v_pk_mul_f32 v[162:163], v[162:163], v[114:115]
	v_pk_fma_f32 v[164:165], v[164:165], v[108:109], v[116:117]
	v_pk_fma_f32 v[162:163], v[162:163], v[110:111], v[118:119]
	v_cvt_pk_bf16_f32 v184, v164, v165
	v_lshlrev_b64 v[234:235], 2, v[74:75]
	v_lshlrev_b32_e32 v180, 16, v184
	v_and_b32_e32 v181, 0xffff0000, v184
	v_sub_f32_e32 v180, v164, v180
	v_sub_f32_e32 v181, v165, v181
	v_cvt_pk_bf16_f32 v185, v162, v163
	v_cvt_pk_bf16_f32 v186, v180, v181
	v_lshl_add_u64 v[230:231], s[24:25], 0, v[234:235]
	v_lshlrev_b32_e32 v180, 16, v185
	v_and_b32_e32 v181, 0xffff0000, v185
	v_sub_f32_e32 v180, v162, v180
	v_sub_f32_e32 v181, v163, v181
	v_cvt_pk_bf16_f32 v187, v180, v181
	v_lshl_add_u64 v[180:181], s[12:13], 0, v[234:235]
	v_lshl_add_u64 v[234:235], s[10:11], 0, v[234:235]
	v_xor_b32_e32 v238, s45, v238
	v_lshlrev_b32_e32 v238, 4, v238
	v_add3_u32 v238, s46, v238, v228
	ds_write_b64 v238, v[184:185]
	v_add_u32_e32 v184, 0x10000, v238
	ds_write_b64 v184, v[186:187]
	v_mov_b32_e32 v184, v148
	v_mov_b32_e32 v185, v150
	v_pk_mul_f32 v[184:185], v[184:185], v[166:167] op_sel_hi:[1,0]
	s_waitcnt vmcnt(5)
	v_pk_add_f32 v[238:239], v[120:121], 1.0 op_sel_hi:[1,0]
	v_mov_b32_e32 v180, v156
	v_mov_b32_e32 v181, v158
	v_pk_mul_f32 v[180:181], v[180:181], v[166:167] op_sel_hi:[1,0]
	v_pk_add_f32 v[122:123], v[122:123], 1.0 op_sel_hi:[1,0]
	s_waitcnt vmcnt(4)
	v_pk_mul_f32 v[186:187], v[184:185], v[124:125]
	v_pk_mul_f32 v[180:181], v[180:181], v[126:127]
	s_waitcnt vmcnt(3)
	v_pk_fma_f32 v[186:187], v[186:187], v[238:239], v[212:213]
	v_pk_fma_f32 v[184:185], v[180:181], v[122:123], v[214:215]
	v_cvt_pk_bf16_f32 v180, v186, v187
	v_mov_b32_e32 v158, v157
	v_lshlrev_b32_e32 v148, 16, v180
	v_sub_f32_e32 v148, v186, v148
	v_and_b32_e32 v150, 0xffff0000, v180
	v_cvt_pk_bf16_f32 v181, v184, v185
	v_sub_f32_e32 v150, v187, v150
	v_cvt_pk_bf16_f32 v240, v148, v150
	v_lshlrev_b32_e32 v148, 16, v181
	v_sub_f32_e32 v148, v184, v148
	v_and_b32_e32 v150, 0xffff0000, v181
	v_sub_f32_e32 v150, v185, v150
	v_cvt_pk_bf16_f32 v241, v148, v150
	v_xor_b32_e32 v148, s43, v246
	v_lshlrev_b32_e32 v148, 4, v148
	v_add3_u32 v148, s44, v148, v228
	ds_write_b64 v148, v[180:181]
	v_add_u32_e32 v148, 0x10000, v148
	ds_write_b64 v148, v[240:241]
	v_mov_b32_e32 v180, v176
	v_mov_b32_e32 v181, v178
	v_mov_b32_e32 v240, v168
	v_mov_b32_e32 v241, v172
	v_pk_mul_f32 v[180:181], v[180:181], v[160:161] op_sel_hi:[1,0]
	v_pk_mul_f32 v[240:241], v[240:241], v[160:161] op_sel_hi:[1,0]
	v_pk_mul_f32 v[180:181], v[180:181], v[126:127]
	v_pk_mul_f32 v[124:125], v[240:241], v[124:125]
	v_pk_fma_f32 v[180:181], v[180:181], v[122:123], v[214:215]
	v_pk_fma_f32 v[182:183], v[124:125], v[238:239], v[212:213]
	v_lshlrev_b64 v[238:239], 2, v[72:73]
	v_cvt_pk_bf16_f32 v242, v182, v183
	v_cvt_pk_bf16_f32 v243, v180, v181
	v_lshl_add_u64 v[230:231], s[12:13], 0, v[238:239]
	v_lshlrev_b32_e32 v148, 16, v242
	v_and_b32_e32 v150, 0xffff0000, v242
	v_sub_f32_e32 v148, v182, v148
	v_sub_f32_e32 v150, v183, v150
	v_cvt_pk_bf16_f32 v244, v148, v150
	v_lshlrev_b32_e32 v148, 16, v243
	v_and_b32_e32 v150, 0xffff0000, v243
	v_lshl_add_u64 v[234:235], s[24:25], 0, v[238:239]
	v_sub_f32_e32 v148, v180, v148
	v_sub_f32_e32 v150, v181, v150
	v_cvt_pk_bf16_f32 v245, v148, v150
	v_lshl_add_u64 v[238:239], s[10:11], 0, v[238:239]
	v_xor_b32_e32 v148, s45, v246
	v_lshlrev_b32_e32 v148, 4, v148
	v_add3_u32 v148, s46, v148, v228
	ds_write_b64 v148, v[242:243]
	v_add_u32_e32 v148, 0x10000, v148
	v_mov_b32_e32 v150, v149
	ds_write_b64 v148, v[244:245]
	v_pk_mul_f32 v[156:157], v[158:159], v[166:167] op_sel_hi:[1,0]
	v_pk_mul_f32 v[148:149], v[150:151], v[166:167] op_sel_hi:[1,0]
	v_add_u32_e32 v242, 0x60, v229
	v_mov_b32_e32 v172, v169
	v_mov_b32_e32 v178, v177
	v_add_u32_e32 v246, 0x80, v229
	s_waitcnt vmcnt(2)
	v_pk_add_f32 v[218:219], v[218:219], 1.0 op_sel_hi:[1,0]
	v_pk_add_f32 v[216:217], v[216:217], 1.0 op_sel_hi:[1,0]
	s_waitcnt vmcnt(1)
	v_pk_mul_f32 v[148:149], v[148:149], v[220:221]
	v_pk_mul_f32 v[150:151], v[156:157], v[222:223]
	s_waitcnt vmcnt(0)
	v_pk_fma_f32 v[158:159], v[148:149], v[216:217], v[224:225]
	v_pk_fma_f32 v[156:157], v[150:151], v[218:219], v[226:227]
	v_cvt_pk_bf16_f32 v148, v158, v159
	s_nop 0
	v_lshlrev_b32_e32 v150, 16, v148
	v_and_b32_e32 v151, 0xffff0000, v148
	v_sub_f32_e32 v150, v158, v150
	v_sub_f32_e32 v151, v159, v151
	v_cvt_pk_bf16_f32 v149, v156, v157
	v_cvt_pk_bf16_f32 v150, v150, v151
	s_nop 0
	v_lshlrev_b32_e32 v151, 16, v149
	v_and_b32_e32 v168, 0xffff0000, v149
	v_sub_f32_e32 v151, v156, v151
	v_sub_f32_e32 v168, v157, v168
	v_cvt_pk_bf16_f32 v151, v151, v168
	v_xor_b32_e32 v168, s43, v242
	v_lshlrev_b32_e32 v168, 4, v168
	v_add3_u32 v168, s44, v168, v228
	ds_write_b64 v168, v[148:149]
	v_add_u32_e32 v148, 0x10000, v168
	ds_write_b64 v148, v[150:151]
	v_pk_mul_f32 v[150:151], v[172:173], v[160:161] op_sel_hi:[1,0]
	v_pk_mul_f32 v[148:149], v[178:179], v[160:161] op_sel_hi:[1,0]
	v_pk_mul_f32 v[150:151], v[150:151], v[220:221]
	v_pk_mul_f32 v[148:149], v[148:149], v[222:223]
	v_pk_fma_f32 v[150:151], v[150:151], v[216:217], v[224:225]
	v_pk_fma_f32 v[148:149], v[148:149], v[218:219], v[226:227]
	v_cvt_pk_bf16_f32 v168, v150, v151
	v_lshlrev_b64 v[234:235], 2, v[70:71]
	v_lshlrev_b32_e32 v172, 16, v168
	v_and_b32_e32 v173, 0xffff0000, v168
	v_sub_f32_e32 v172, v150, v172
	v_sub_f32_e32 v173, v151, v173
	v_cvt_pk_bf16_f32 v169, v148, v149
	v_cvt_pk_bf16_f32 v172, v172, v173
	v_lshl_add_u64 v[230:231], s[24:25], 0, v[234:235]
	v_lshlrev_b32_e32 v173, 16, v169
	v_and_b32_e32 v176, 0xffff0000, v169
	v_sub_f32_e32 v173, v148, v173
	v_sub_f32_e32 v176, v149, v176
	v_cvt_pk_bf16_f32 v173, v173, v176
	v_lshl_add_u64 v[176:177], s[12:13], 0, v[234:235]
	global_load_dwordx4 v[96:99], v251, s[12:13]
	global_load_dwordx4 v[100:103], v251, s[24:25]
	global_load_dwordx4 v[104:107], v251, s[10:11]
	global_load_dwordx4 v[108:111], v251, s[12:13] offset:1024
	global_load_dwordx4 v[112:115], v251, s[24:25] offset:1024
	global_load_dwordx4 v[116:119], v251, s[10:11] offset:1024
	global_load_dwordx4 v[120:123], v251, s[12:13] offset:2048
	global_load_dwordx4 v[124:127], v251, s[24:25] offset:2048
	global_load_dwordx4 v[212:215], v251, s[10:11] offset:2048
	global_load_dwordx4 v[216:219], v251, s[12:13] offset:3072
	global_load_dwordx4 v[220:223], v251, s[24:25] offset:3072
	global_load_dwordx4 v[224:227], v251, s[10:11] offset:3072
	v_lshl_add_u64 v[234:235], s[10:11], 0, v[234:235]
	v_xor_b32_e32 v238, s45, v242
	v_lshlrev_b32_e32 v238, 4, v238
	v_add3_u32 v238, s46, v238, v228
	ds_write_b64 v238, v[168:169]
	v_add_u32_e32 v168, 0x10000, v238
	ds_write_b64 v168, v[172:173]
	s_waitcnt vmcnt(11)
	v_pk_add_f32 v[168:169], v[98:99], 1.0 op_sel_hi:[1,0]
	v_mov_b32_e32 v178, v92
	v_mov_b32_e32 v179, v94
	v_pk_mul_f32 v[178:179], v[178:179], v[166:167] op_sel_hi:[1,0]
	v_pk_add_f32 v[172:173], v[96:97], 1.0 op_sel_hi:[1,0]
	v_mov_b32_e32 v176, v130
	v_mov_b32_e32 v177, v134
	s_waitcnt vmcnt(10)
	v_pk_mul_f32 v[178:179], v[178:179], v[100:101]
	v_pk_mul_f32 v[176:177], v[176:177], v[166:167] op_sel_hi:[1,0]
	s_waitcnt vmcnt(9)
	v_pk_fma_f32 v[178:179], v[178:179], v[172:173], v[104:105]
	v_pk_mul_f32 v[176:177], v[176:177], v[102:103]
	v_cvt_pk_bf16_f32 v238, v178, v179
	v_mov_b32_e32 v134, v131
	v_lshlrev_b32_e32 v92, 16, v238
	v_sub_f32_e32 v92, v178, v92
	v_and_b32_e32 v94, 0xffff0000, v238
	v_pk_fma_f32 v[176:177], v[176:177], v[168:169], v[106:107]
	v_sub_f32_e32 v94, v179, v94
	v_cvt_pk_bf16_f32 v239, v176, v177
	v_cvt_pk_bf16_f32 v240, v92, v94
	v_pk_mul_f32 v[130:131], v[134:135], v[166:167] op_sel_hi:[1,0]
	v_lshlrev_b32_e32 v92, 16, v239
	v_sub_f32_e32 v92, v176, v92
	v_and_b32_e32 v94, 0xffff0000, v239
	v_sub_f32_e32 v94, v177, v94
	v_cvt_pk_bf16_f32 v241, v92, v94
	v_xor_b32_e32 v92, s43, v246
	v_lshlrev_b32_e32 v92, 4, v92
	v_add3_u32 v92, s44, v92, v228
	ds_write_b64 v92, v[238:239]
	v_add_u32_e32 v92, 0x10000, v92
	ds_write_b64 v92, v[240:241]
	v_mov_b32_e32 v240, v138
	v_mov_b32_e32 v241, v140
	v_pk_mul_f32 v[240:241], v[240:241], v[160:161] op_sel_hi:[1,0]
	v_mov_b32_e32 v238, v142
	v_mov_b32_e32 v239, v144
	v_pk_mul_f32 v[100:101], v[240:241], v[100:101]
	v_pk_mul_f32 v[238:239], v[238:239], v[160:161] op_sel_hi:[1,0]
	v_pk_fma_f32 v[172:173], v[100:101], v[172:173], v[104:105]
	v_pk_mul_f32 v[102:103], v[238:239], v[102:103]
	v_cvt_pk_bf16_f32 v242, v172, v173
	v_lshlrev_b64 v[238:239], 2, v[68:69]
	v_lshlrev_b32_e32 v92, 16, v242
	v_and_b32_e32 v94, 0xffff0000, v242
	v_sub_f32_e32 v92, v172, v92
	v_sub_f32_e32 v94, v173, v94
	v_pk_fma_f32 v[168:169], v[102:103], v[168:169], v[106:107]
	v_lshl_add_u64 v[230:231], s[12:13], 0, v[238:239]
	v_cvt_pk_bf16_f32 v243, v168, v169
	v_cvt_pk_bf16_f32 v244, v92, v94
	v_lshl_add_u64 v[234:235], s[24:25], 0, v[238:239]
	v_lshlrev_b32_e32 v92, 16, v243
	v_and_b32_e32 v94, 0xffff0000, v243
	v_sub_f32_e32 v92, v168, v92
	v_sub_f32_e32 v94, v169, v94
	v_cvt_pk_bf16_f32 v245, v92, v94
	v_lshl_add_u64 v[238:239], s[10:11], 0, v[238:239]
	v_xor_b32_e32 v92, s45, v246
	v_lshlrev_b32_e32 v92, 4, v92
	v_add3_u32 v92, s46, v92, v228
	ds_write_b64 v92, v[242:243]
	v_add_u32_e32 v92, 0x10000, v92
	v_mov_b32_e32 v94, v93
	ds_write_b64 v92, v[244:245]
	v_pk_mul_f32 v[92:93], v[94:95], v[166:167] op_sel_hi:[1,0]
	v_add_u32_e32 v242, 0xa0, v229
	v_mov_b32_e32 v140, v139
	v_mov_b32_e32 v144, v143
	v_add_u32_e32 v246, 0xc0, v229
	s_waitcnt vmcnt(8)
	v_pk_add_f32 v[110:111], v[110:111], 1.0 op_sel_hi:[1,0]
	v_pk_add_f32 v[108:109], v[108:109], 1.0 op_sel_hi:[1,0]
	s_waitcnt vmcnt(7)
	v_pk_mul_f32 v[92:93], v[92:93], v[112:113]
	v_pk_mul_f32 v[94:95], v[130:131], v[114:115]
	s_waitcnt vmcnt(6)
	v_pk_fma_f32 v[134:135], v[92:93], v[108:109], v[116:117]
	v_pk_fma_f32 v[130:131], v[94:95], v[110:111], v[118:119]
	v_cvt_pk_bf16_f32 v92, v134, v135
	s_nop 0
	v_lshlrev_b32_e32 v94, 16, v92
	v_and_b32_e32 v95, 0xffff0000, v92
	v_sub_f32_e32 v94, v134, v94
	v_sub_f32_e32 v95, v135, v95
	v_cvt_pk_bf16_f32 v93, v130, v131
	v_cvt_pk_bf16_f32 v94, v94, v95
	s_nop 0
	v_lshlrev_b32_e32 v95, 16, v93
	v_and_b32_e32 v138, 0xffff0000, v93
	v_sub_f32_e32 v95, v130, v95
	v_sub_f32_e32 v138, v131, v138
	v_cvt_pk_bf16_f32 v95, v95, v138
	v_xor_b32_e32 v138, s43, v242
	v_lshlrev_b32_e32 v138, 4, v138
	v_add3_u32 v138, s44, v138, v228
	ds_write_b64 v138, v[92:93]
	v_add_u32_e32 v92, 0x10000, v138
	ds_write_b64 v92, v[94:95]
	v_pk_mul_f32 v[94:95], v[140:141], v[160:161] op_sel_hi:[1,0]
	v_pk_mul_f32 v[92:93], v[144:145], v[160:161] op_sel_hi:[1,0]
	v_pk_mul_f32 v[94:95], v[94:95], v[112:113]
	v_pk_mul_f32 v[92:93], v[92:93], v[114:115]
	v_pk_fma_f32 v[94:95], v[94:95], v[108:109], v[116:117]
	v_pk_fma_f32 v[92:93], v[92:93], v[110:111], v[118:119]
	v_cvt_pk_bf16_f32 v234, v94, v95
	v_lshlrev_b64 v[230:231], 2, v[66:67]
	v_lshlrev_b32_e32 v138, 16, v234
	v_and_b32_e32 v139, 0xffff0000, v234
	v_sub_f32_e32 v138, v94, v138
	v_sub_f32_e32 v139, v95, v139
	v_cvt_pk_bf16_f32 v235, v92, v93
	v_cvt_pk_bf16_f32 v236, v138, v139
	v_lshl_add_u64 v[142:143], s[24:25], 0, v[230:231]
	v_lshlrev_b32_e32 v138, 16, v235
	v_and_b32_e32 v139, 0xffff0000, v235
	v_sub_f32_e32 v138, v92, v138
	v_sub_f32_e32 v139, v93, v139
	v_cvt_pk_bf16_f32 v237, v138, v139
	v_lshl_add_u64 v[138:139], s[12:13], 0, v[230:231]
	v_lshl_add_u64 v[230:231], s[10:11], 0, v[230:231]
	v_xor_b32_e32 v238, s45, v242
	v_lshlrev_b32_e32 v238, 4, v238
	v_add3_u32 v238, s46, v238, v228
	ds_write_b64 v238, v[234:235]
	v_add_u32_e32 v234, 0x10000, v238
	ds_write_b64 v234, v[236:237]
	v_mov_b32_e32 v236, v80
	v_mov_b32_e32 v237, v82
	v_pk_mul_f32 v[236:237], v[236:237], v[166:167] op_sel_hi:[1,0]
	s_waitcnt vmcnt(5)
	v_pk_add_f32 v[234:235], v[120:121], 1.0 op_sel_hi:[1,0]
	v_mov_b32_e32 v138, v84
	v_mov_b32_e32 v139, v86
	v_pk_mul_f32 v[138:139], v[138:139], v[166:167] op_sel_hi:[1,0]
	v_pk_add_f32 v[122:123], v[122:123], 1.0 op_sel_hi:[1,0]
	s_waitcnt vmcnt(4)
	v_pk_mul_f32 v[236:237], v[236:237], v[124:125]
	v_pk_mul_f32 v[138:139], v[138:139], v[126:127]
	s_waitcnt vmcnt(3)
	v_pk_fma_f32 v[240:241], v[236:237], v[234:235], v[212:213]
	v_pk_fma_f32 v[238:239], v[138:139], v[122:123], v[214:215]
	v_cvt_pk_bf16_f32 v138, v240, v241
	v_mov_b32_e32 v86, v85
	v_lshlrev_b32_e32 v80, 16, v138
	v_sub_f32_e32 v80, v240, v80
	v_and_b32_e32 v82, 0xffff0000, v138
	v_cvt_pk_bf16_f32 v139, v238, v239
	v_sub_f32_e32 v82, v241, v82
	v_cvt_pk_bf16_f32 v236, v80, v82
	v_lshlrev_b32_e32 v80, 16, v139
	v_sub_f32_e32 v80, v238, v80
	v_and_b32_e32 v82, 0xffff0000, v139
	v_sub_f32_e32 v82, v239, v82
	v_cvt_pk_bf16_f32 v237, v80, v82
	v_xor_b32_e32 v80, s43, v246
	v_lshlrev_b32_e32 v80, 4, v80
	v_add3_u32 v80, s44, v80, v228
	ds_write_b64 v80, v[138:139]
	v_add_u32_e32 v80, 0x10000, v80
	ds_write_b64 v80, v[236:237]
	v_mov_b32_e32 v138, v128
	v_mov_b32_e32 v139, v132
	v_mov_b32_e32 v236, v88
	v_mov_b32_e32 v237, v90
	v_pk_mul_f32 v[138:139], v[138:139], v[160:161] op_sel_hi:[1,0]
	v_pk_mul_f32 v[236:237], v[236:237], v[160:161] op_sel_hi:[1,0]
	v_pk_mul_f32 v[138:139], v[138:139], v[126:127]
	v_pk_mul_f32 v[124:125], v[236:237], v[124:125]
	v_pk_fma_f32 v[138:139], v[138:139], v[122:123], v[214:215]
	v_pk_fma_f32 v[140:141], v[124:125], v[234:235], v[212:213]
	v_lshlrev_b64 v[234:235], 2, v[64:65]
	v_cvt_pk_bf16_f32 v242, v140, v141
	v_cvt_pk_bf16_f32 v243, v138, v139
	v_lshl_add_u64 v[142:143], s[12:13], 0, v[234:235]
	v_lshlrev_b32_e32 v80, 16, v242
	v_and_b32_e32 v82, 0xffff0000, v242
	v_sub_f32_e32 v80, v140, v80
	v_sub_f32_e32 v82, v141, v82
	v_cvt_pk_bf16_f32 v244, v80, v82
	v_lshlrev_b32_e32 v80, 16, v243
	v_and_b32_e32 v82, 0xffff0000, v243
	v_lshl_add_u64 v[230:231], s[24:25], 0, v[234:235]
	v_sub_f32_e32 v80, v138, v80
	v_sub_f32_e32 v82, v139, v82
	v_cvt_pk_bf16_f32 v245, v80, v82
	v_lshl_add_u64 v[234:235], s[10:11], 0, v[234:235]
	v_xor_b32_e32 v80, s45, v246
	v_lshlrev_b32_e32 v80, 4, v80
	v_add3_u32 v80, s46, v80, v228
	ds_write_b64 v80, v[242:243]
	v_add_u32_e32 v80, 0x10000, v80
	v_mov_b32_e32 v82, v81
	ds_write_b64 v80, v[244:245]
	v_pk_mul_f32 v[80:81], v[82:83], v[166:167] op_sel_hi:[1,0]
	v_pk_mul_f32 v[84:85], v[86:87], v[166:167] op_sel_hi:[1,0]
	v_add_u32_e32 v128, 0xe0, v229
	v_mov_b32_e32 v90, v89
	v_mov_b32_e32 v132, v129
	s_waitcnt vmcnt(2)
	v_pk_add_f32 v[216:217], v[216:217], 1.0 op_sel_hi:[1,0]
	v_pk_add_f32 v[218:219], v[218:219], 1.0 op_sel_hi:[1,0]
	s_waitcnt vmcnt(1)
	v_pk_mul_f32 v[80:81], v[80:81], v[220:221]
	v_pk_mul_f32 v[82:83], v[84:85], v[222:223]
	s_waitcnt vmcnt(0)
	v_pk_fma_f32 v[80:81], v[80:81], v[216:217], v[224:225]
	v_pk_fma_f32 v[82:83], v[82:83], v[218:219], v[226:227]
	v_cvt_pk_bf16_f32 v84, v80, v81
	s_nop 0
	v_lshlrev_b32_e32 v86, 16, v84
	v_and_b32_e32 v87, 0xffff0000, v84
	v_sub_f32_e32 v86, v80, v86
	v_sub_f32_e32 v87, v81, v87
	v_cvt_pk_bf16_f32 v85, v82, v83
	v_cvt_pk_bf16_f32 v86, v86, v87
	s_nop 0
	v_lshlrev_b32_e32 v87, 16, v85
	v_and_b32_e32 v88, 0xffff0000, v85
	v_sub_f32_e32 v87, v82, v87
	v_sub_f32_e32 v88, v83, v88
	v_cvt_pk_bf16_f32 v87, v87, v88
	v_xor_b32_e32 v88, s43, v128
	v_lshlrev_b32_e32 v88, 4, v88
	v_add3_u32 v88, s44, v88, v228
	ds_write_b64 v88, v[84:85]
	v_add_u32_e32 v84, 0x10000, v88
	ds_write_b64 v84, v[86:87]
	v_pk_mul_f32 v[86:87], v[90:91], v[160:161] op_sel_hi:[1,0]
	v_pk_mul_f32 v[84:85], v[132:133], v[160:161] op_sel_hi:[1,0]
	v_pk_mul_f32 v[86:87], v[86:87], v[220:221]
	v_pk_mul_f32 v[84:85], v[84:85], v[222:223]
	v_pk_fma_f32 v[86:87], v[86:87], v[216:217], v[224:225]
	v_xor_b32_e32 v128, s45, v128
	v_cvt_pk_bf16_f32 v88, v86, v87
	v_pk_fma_f32 v[84:85], v[84:85], v[218:219], v[226:227]
	s_cmp_lt_i32 s56, s39
	s_cbranch_scc0 .Lpf_skip_0
	s_add_i32 s98, s38, s18
	s_ashr_i32 s99, s98, 31
	s_lshl_b64 s[100:101], s[98:99], 11
	s_lshl_b64 s[98:99], s[98:99], 12
	s_add_u32 s98, s35, s98
	s_addc_u32 s99, s36, s99
	s_add_u32 s100, s37, s100
	v_lshlrev_b64 v[112:113], 1, v[78:79]
	s_addc_u32 s101, s40, s101
	v_lshl_add_u64 v[110:111], s[98:99], 0, v[112:113]
	s_add_i32 s98, s47, s18
	s_ashr_i32 s99, s98, 31
	v_lshl_add_u64 v[114:115], s[100:101], 0, v[78:79]
	s_lshl_b64 s[100:101], s[98:99], 11
	s_lshl_b64 s[98:99], s[98:99], 12
	s_add_u32 s98, s35, s98
	s_addc_u32 s99, s36, s99
	s_add_u32 s100, s37, s100
	s_addc_u32 s101, s40, s101
	v_lshl_add_u64 v[126:127], s[98:99], 0, v[112:113]
	global_load_dwordx2 v[96:97], v[110:111], off
	global_load_dwordx2 v[98:99], v[110:111], off offset:512
	global_load_dwordx2 v[100:101], v[110:111], off offset:1024
	global_load_dwordx2 v[102:103], v[110:111], off offset:1536
	global_load_dwordx2 v[104:105], v[110:111], off offset:2048
	global_load_dwordx2 v[106:107], v[110:111], off offset:2560
	global_load_dwordx2 v[108:109], v[110:111], off offset:3072
	s_nop 0
	global_load_dwordx2 v[110:111], v[110:111], off offset:3584
	s_nop 0
	global_load_dword v212, v[114:115], off
	global_load_dword v213, v[114:115], off offset:256
	global_load_dword v214, v[114:115], off offset:512
	global_load_dword v215, v[114:115], off offset:768
	global_load_dword v216, v[114:115], off offset:1024
	global_load_dword v217, v[114:115], off offset:1280
	global_load_dword v218, v[114:115], off offset:1536
	global_load_dword v219, v[114:115], off offset:1792
	v_lshl_add_u64 v[250:251], s[100:101], 0, v[78:79]
	global_load_dwordx2 v[112:113], v[126:127], off
	global_load_dwordx2 v[114:115], v[126:127], off offset:512
	global_load_dwordx2 v[116:117], v[126:127], off offset:1024
	global_load_dwordx2 v[118:119], v[126:127], off offset:1536
	global_load_dwordx2 v[120:121], v[126:127], off offset:2048
	global_load_dwordx2 v[122:123], v[126:127], off offset:2560
	global_load_dwordx2 v[124:125], v[126:127], off offset:3072
	s_nop 0
	global_load_dwordx2 v[126:127], v[126:127], off offset:3584
	s_nop 0
	global_load_dword v220, v[250:251], off
	global_load_dword v221, v[250:251], off offset:256
	global_load_dword v222, v[250:251], off offset:512
	global_load_dword v223, v[250:251], off offset:768
	global_load_dword v224, v[250:251], off offset:1024
	global_load_dword v225, v[250:251], off offset:1280
	global_load_dword v226, v[250:251], off offset:1536
	global_load_dword v227, v[250:251], off offset:1792
.Lpf_skip_0:
	v_lshlrev_b32_e32 v90, 16, v88
	v_and_b32_e32 v91, 0xffff0000, v88
	v_sub_f32_e32 v90, v86, v90
	v_sub_f32_e32 v91, v87, v91
	v_cvt_pk_bf16_f32 v89, v84, v85
	v_cvt_pk_bf16_f32 v90, v90, v91
	v_lshlrev_b32_e32 v128, 4, v128
	v_lshlrev_b32_e32 v91, 16, v89
	v_sub_f32_e32 v91, v84, v91
	v_and_b32_e32 v129, 0xffff0000, v89
	v_add3_u32 v128, s46, v128, v228
	v_sub_f32_e32 v129, v85, v129
	v_cvt_pk_bf16_f32 v91, v91, v129
	ds_write_b64 v128, v[88:89]
	v_add_u32_e32 v88, 0x10000, v128
	ds_write_b64 v88, v[90:91]
	v_mov_b32_e32 v90, 0
	v_cvt_pk_fp8_f32 v90, v154, v155
	v_mov_b32_e32 v91, 0
	v_cvt_pk_fp8_f32 v91, v174, v175
	v_lshl_add_u64 v[88:89], s[6:7], 0, v[78:79]
	v_cvt_pk_fp8_f32 v90, v152, v153 op_sel:[0,0,1]
	v_mov_b32_e32 v128, 0
	v_cvt_pk_fp8_f32 v91, v170, v171 op_sel:[0,0,1]
	v_cvt_pk_fp8_f32 v128, v186, v187
	global_store_dword v[88:89], v90, off
	v_lshl_add_u64 v[88:89], s[6:7], 0, v[76:77]
	v_mov_b32_e32 v90, 0
	global_store_dword v[88:89], v91, off
	v_cvt_pk_fp8_f32 v90, v158, v159
	v_mov_b32_e32 v91, 0
	v_cvt_pk_fp8_f32 v91, v178, v179
	v_cvt_pk_fp8_f32 v128, v184, v185 op_sel:[0,0,1]
	v_cvt_pk_fp8_f32 v90, v156, v157 op_sel:[0,0,1]
	v_lshl_add_u64 v[88:89], s[6:7], 0, v[74:75]
	v_cvt_pk_fp8_f32 v91, v176, v177 op_sel:[0,0,1]
	global_store_dword v[88:89], v128, off
	v_lshl_add_u64 v[88:89], s[6:7], 0, v[72:73]
	v_mov_b32_e32 v128, 0
	global_store_dword v[88:89], v90, off
	v_lshl_add_u64 v[88:89], s[6:7], 0, v[70:71]
	v_cvt_pk_fp8_f32 v128, v134, v135
	global_store_dword v[88:89], v91, off
	v_mov_b32_e32 v88, 0
	v_cvt_pk_fp8_f32 v88, v240, v241
	v_mov_b32_e32 v89, 0
	v_cvt_pk_fp8_f32 v89, v80, v81
	v_cvt_pk_fp8_f32 v128, v130, v131 op_sel:[0,0,1]
	v_cvt_pk_fp8_f32 v88, v238, v239 op_sel:[0,0,1]
	v_lshl_add_u64 v[80:81], s[6:7], 0, v[68:69]
	v_cvt_pk_fp8_f32 v89, v82, v83 op_sel:[0,0,1]
	global_store_dword v[80:81], v128, off
	v_lshl_add_u64 v[80:81], s[6:7], 0, v[66:67]
	global_store_dword v[80:81], v88, off
	v_lshl_add_u64 v[80:81], s[6:7], 0, v[64:65]
	global_store_dword v[80:81], v89, off
	v_mov_b32_e32 v80, 0
	v_mov_b32_e32 v81, 0
	v_cvt_pk_fp8_f32 v80, v146, v147
	v_cvt_pk_fp8_f32 v81, v164, v165
	s_add_i32 s6, s1, s18
	s_ashr_i32 s7, s6, 31
	s_lshl_b64 s[6:7], s[6:7], 11
	v_cvt_pk_fp8_f32 v80, v136, v137 op_sel:[0,0,1]
	v_cvt_pk_fp8_f32 v81, v162, v163 op_sel:[0,0,1]
	s_add_u32 s6, s41, s6
	s_addc_u32 s7, s42, s7
	v_lshl_add_u64 v[78:79], s[6:7], 0, v[78:79]
	v_lshl_add_u64 v[76:77], s[6:7], 0, v[76:77]
	v_mov_b32_e32 v82, 0
	global_store_dword v[78:79], v80, off
	global_store_dword v[76:77], v81, off
	v_mov_b32_e32 v76, 0
	v_mov_b32_e32 v77, 0
	v_cvt_pk_fp8_f32 v82, v182, v183
	v_cvt_pk_fp8_f32 v76, v150, v151
	v_cvt_pk_fp8_f32 v77, v172, v173
	v_lshl_add_u64 v[74:75], s[6:7], 0, v[74:75]
	v_cvt_pk_fp8_f32 v82, v180, v181 op_sel:[0,0,1]
	v_cvt_pk_fp8_f32 v76, v148, v149 op_sel:[0,0,1]
	v_cvt_pk_fp8_f32 v77, v168, v169 op_sel:[0,0,1]
	v_lshl_add_u64 v[72:73], s[6:7], 0, v[72:73]
	v_lshl_add_u64 v[70:71], s[6:7], 0, v[70:71]
	global_store_dword v[74:75], v82, off
	v_mov_b32_e32 v74, 0
	global_store_dword v[72:73], v76, off
	global_store_dword v[70:71], v77, off
	v_mov_b32_e32 v70, 0
	v_mov_b32_e32 v71, 0
	v_cvt_pk_fp8_f32 v74, v94, v95
	v_cvt_pk_fp8_f32 v70, v140, v141
	v_cvt_pk_fp8_f32 v71, v86, v87
	v_lshl_add_u64 v[68:69], s[6:7], 0, v[68:69]
	v_cvt_pk_fp8_f32 v74, v92, v93 op_sel:[0,0,1]
	v_cvt_pk_fp8_f32 v70, v138, v139 op_sel:[0,0,1]
	v_cvt_pk_fp8_f32 v71, v84, v85 op_sel:[0,0,1]
	v_lshl_add_u64 v[66:67], s[6:7], 0, v[66:67]
	v_lshl_add_u64 v[64:65], s[6:7], 0, v[64:65]
	global_store_dword v[68:69], v74, off
	global_store_dword v[66:67], v70, off
	global_store_dword v[64:65], v71, off
	s_waitcnt lgkmcnt(0)
	s_barrier
	ds_read_b128 v[64:67], v190
	ds_read_b128 v[68:71], v191
	s_waitcnt lgkmcnt(1)
	v_mfma_f32_16x16x32_bf16 v[72:75], v[0:3], v[64:67], 0
	v_mov_b32_e32 v128, v167
	v_mfma_f32_16x16x32_bf16 v[64:67], v[4:7], v[64:67], v[72:75]
	s_waitcnt lgkmcnt(0)
	v_mfma_f32_16x16x32_bf16 v[64:67], v[0:3], v[68:71], v[64:67]
	ds_read_b128 v[68:71], v192
	s_nop 2
	ds_read_b128 v[72:75], v193
	s_waitcnt lgkmcnt(1)
	v_mfma_f32_16x16x32_bf16 v[64:67], v[8:11], v[68:71], v[64:67]
	v_mfma_f32_16x16x32_bf16 v[64:67], v[12:15], v[68:71], v[64:67]
	s_waitcnt lgkmcnt(0)
	v_mfma_f32_16x16x32_bf16 v[64:67], v[8:11], v[72:75], v[64:67]
	ds_read_b128 v[68:71], v194
	ds_read_b128 v[72:75], v195
	s_waitcnt lgkmcnt(1)
	v_mfma_f32_16x16x32_bf16 v[64:67], v[16:19], v[68:71], v[64:67]
	v_mfma_f32_16x16x32_bf16 v[64:67], v[20:23], v[68:71], v[64:67]
	s_waitcnt lgkmcnt(0)
	v_mfma_f32_16x16x32_bf16 v[64:67], v[16:19], v[72:75], v[64:67]
	ds_read_b128 v[68:71], v196
	ds_read_b128 v[72:75], v197
	s_waitcnt lgkmcnt(1)
	v_mfma_f32_16x16x32_bf16 v[64:67], v[24:27], v[68:71], v[64:67]
	v_mfma_f32_16x16x32_bf16 v[64:67], v[28:31], v[68:71], v[64:67]
	s_waitcnt lgkmcnt(0)
	v_mfma_f32_16x16x32_bf16 v[64:67], v[24:27], v[72:75], v[64:67]
	ds_read_b128 v[68:71], v198
	ds_read_b128 v[72:75], v199
	s_waitcnt lgkmcnt(1)
	v_mfma_f32_16x16x32_bf16 v[64:67], v[32:35], v[68:71], v[64:67]
	v_mfma_f32_16x16x32_bf16 v[64:67], v[36:39], v[68:71], v[64:67]
	s_waitcnt lgkmcnt(0)
	v_mfma_f32_16x16x32_bf16 v[64:67], v[32:35], v[72:75], v[64:67]
	ds_read_b128 v[68:71], v200
	ds_read_b128 v[72:75], v201
	s_waitcnt lgkmcnt(1)
	v_mfma_f32_16x16x32_bf16 v[64:67], v[40:43], v[68:71], v[64:67]
	v_mfma_f32_16x16x32_bf16 v[64:67], v[44:47], v[68:71], v[64:67]
	s_waitcnt lgkmcnt(0)
	v_mfma_f32_16x16x32_bf16 v[64:67], v[40:43], v[72:75], v[64:67]
	ds_read_b128 v[68:71], v202
	ds_read_b128 v[72:75], v203
	s_waitcnt lgkmcnt(1)
	v_mfma_f32_16x16x32_bf16 v[64:67], v[48:51], v[68:71], v[64:67]
	v_mfma_f32_16x16x32_bf16 v[64:67], v[52:55], v[68:71], v[64:67]
	s_waitcnt lgkmcnt(0)
	v_mfma_f32_16x16x32_bf16 v[64:67], v[48:51], v[72:75], v[64:67]
	ds_read_b128 v[68:71], v204
	ds_read_b128 v[72:75], v205
	s_waitcnt lgkmcnt(1)
	v_mfma_f32_16x16x32_bf16 v[64:67], v[56:59], v[68:71], v[64:67]
	v_mfma_f32_16x16x32_bf16 v[64:67], v[60:63], v[68:71], v[64:67]
	s_waitcnt lgkmcnt(0)
	v_mfma_f32_16x16x32_bf16 v[64:67], v[56:59], v[72:75], v[64:67]
	s_nop 7
	ds_write_b128 v208, v[64:67]
	s_waitcnt lgkmcnt(0)
	s_barrier
	s_nop 0
	v_cmp_gt_i32_e32 vcc, s48, v128
	s_and_saveexec_b64 s[6:7], vcc
	s_cbranch_execz .LBB0_1743
	v_lshl_add_u32 v72, v128, 2, 0
	v_add_u32_e32 v70, 0x22000, v72
	ds_read2st64_b32 v[64:65], v70 offset1:4
	ds_read2st64_b32 v[66:67], v70 offset0:8 offset1:12
	ds_read2st64_b32 v[68:69], v70 offset0:16 offset1:20
	ds_read2st64_b32 v[70:71], v70 offset0:24 offset1:28
	s_waitcnt lgkmcnt(3)
	v_add_f32_e32 v64, 0, v64
	v_add_f32_e32 v64, v64, v65
	s_waitcnt lgkmcnt(2)
	v_add_f32_e32 v64, v64, v66
	v_add_f32_e32 v64, v64, v67
	s_waitcnt lgkmcnt(1)
	v_add_f32_e32 v64, v64, v68
	v_add_f32_e32 v64, v64, v69
	s_waitcnt lgkmcnt(0)
	v_add_f32_e32 v64, v64, v70
	v_add_f32_e32 v64, v64, v71
	v_add_u32_e32 v65, 0x21000, v72
	ds_write_b32 v65, v64

.LBB0_5165:
	s_or_b64 exec, exec, s[28:29]
	s_waitcnt vmcnt(0)
	s_add_i32 s34, s34, 2
	s_add_i32 s18, s18, s38
	s_cmp_eq_u32 s39, s56
	v_mov_b32_e32 v134, v217
	v_mov_b32_e32 v135, v216
	v_mov_b32_e32 v148, v215
	v_mov_b32_e32 v149, v214
	v_mov_b32_e32 v150, v213
	v_mov_b32_e32 v146, v212
	v_mov_b32_e32 v173, v218
	v_mov_b32_e32 v171, v219
	v_mov_b32_e32 v170, v220
	v_mov_b32_e32 v172, v221
	v_mov_b32_e32 v169, v222
	v_mov_b32_e32 v168, v223
	v_mov_b32_e32 v166, v224
	v_mov_b32_e32 v160, v225
	v_mov_b32_e32 v155, v226
	v_mov_b32_e32 v154, v227
	v_mov_b64_e32 v[130:131], v[96:97]
	v_mov_b64_e32 v[94:95], v[98:99]
	v_mov_b64_e32 v[84:85], v[100:101]
	v_mov_b64_e32 v[92:93], v[102:103]
	v_mov_b64_e32 v[80:81], v[104:105]
	v_mov_b64_e32 v[82:83], v[106:107]
	v_mov_b64_e32 v[86:87], v[108:109]
	v_mov_b64_e32 v[144:145], v[110:111]
	v_mov_b64_e32 v[140:141], v[112:113]
	v_mov_b64_e32 v[138:139], v[114:115]
	v_mov_b64_e32 v[128:129], v[116:117]
	v_mov_b64_e32 v[136:137], v[118:119]
	v_mov_b64_e32 v[88:89], v[120:121]
	v_mov_b64_e32 v[90:91], v[122:123]
	v_mov_b64_e32 v[132:133], v[124:125]
	v_mov_b64_e32 v[142:143], v[126:127]
	s_cbranch_scc1 .LBB0_5287

.LBB0_5168:
	s_andn2_b64 vcc, exec, s[6:7]
	s_waitcnt vmcnt(9)
	v_mov_b32_e32 v217, v134
	s_waitcnt vmcnt(8)
	v_mov_b32_e32 v216, v135
	s_waitcnt vmcnt(7)
	v_mov_b32_e32 v215, v148
	s_waitcnt vmcnt(6)
	v_mov_b32_e32 v214, v149
	s_waitcnt vmcnt(5)
	v_mov_b32_e32 v213, v150
	s_waitcnt vmcnt(4)
	v_mov_b32_e32 v212, v146
	v_mov_b32_e32 v218, v173
	v_mov_b32_e32 v219, v171
	v_mov_b32_e32 v220, v170
	v_mov_b32_e32 v221, v172
	v_mov_b32_e32 v222, v169
	v_mov_b32_e32 v223, v168
	v_mov_b32_e32 v224, v166
	v_mov_b32_e32 v225, v160
	v_mov_b32_e32 v226, v155
	v_mov_b32_e32 v227, v154
	s_waitcnt vmcnt(0)
	v_mov_b64_e32 v[96:97], v[130:131]
	v_mov_b64_e32 v[98:99], v[94:95]
	v_mov_b64_e32 v[100:101], v[84:85]
	v_mov_b64_e32 v[102:103], v[92:93]
	v_mov_b64_e32 v[104:105], v[80:81]
	v_mov_b64_e32 v[106:107], v[82:83]
	v_mov_b64_e32 v[108:109], v[86:87]
	v_mov_b64_e32 v[110:111], v[144:145]
	v_mov_b64_e32 v[112:113], v[140:141]
	v_mov_b64_e32 v[114:115], v[138:139]
	v_mov_b64_e32 v[116:117], v[128:129]
	v_mov_b64_e32 v[118:119], v[136:137]
	v_mov_b64_e32 v[120:121], v[88:89]
	v_mov_b64_e32 v[122:123], v[90:91]
	v_mov_b64_e32 v[124:125], v[132:133]
	v_mov_b64_e32 v[126:127], v[142:143]
	v_ashrrev_i32_e32 v77, 31, v76
	v_ashrrev_i32_e32 v75, 31, v74
	v_ashrrev_i32_e32 v73, 31, v72
	v_ashrrev_i32_e32 v71, 31, v70
	v_ashrrev_i32_e32 v69, 31, v68
	v_ashrrev_i32_e32 v67, 31, v66
	v_ashrrev_i32_e32 v65, 31, v64
.LBB0_5170:
	v_cvt_pk_f32_fp8_e32 v[152:153], v146
	v_cvt_pk_f32_fp8_sdwa v[156:157], v146 src0_sel:WORD_1
	v_lshlrev_b32_e32 v146, 16, v130
	v_and_b32_e32 v147, 0xffff0000, v130
	v_lshlrev_b32_e32 v130, 16, v131
	v_and_b32_e32 v131, 0xffff0000, v131
	v_pk_add_f32 v[146:147], v[152:153], v[146:147]
	v_pk_add_f32 v[152:153], v[156:157], v[130:131]
	v_cvt_pk_f32_fp8_e32 v[130:131], v150
	v_cvt_pk_f32_fp8_sdwa v[150:151], v150 src0_sel:WORD_1
	v_lshlrev_b32_e32 v156, 16, v94
	v_and_b32_e32 v157, 0xffff0000, v94
	v_lshlrev_b32_e32 v94, 16, v95
	v_and_b32_e32 v95, 0xffff0000, v95
	v_pk_add_f32 v[164:165], v[150:151], v[94:95]
	v_cvt_pk_f32_fp8_e32 v[94:95], v149
	v_cvt_pk_f32_fp8_e32 v[150:151], v148
	v_pk_add_f32 v[162:163], v[130:131], v[156:157]
	v_cvt_pk_f32_fp8_sdwa v[130:131], v149 src0_sel:WORD_1
	v_cvt_pk_f32_fp8_sdwa v[158:159], v148 src0_sel:WORD_1
	v_lshlrev_b32_e32 v149, 16, v92
	v_lshlrev_b32_e32 v148, 16, v84
	v_mov_b32_e32 v156, v94
	v_mov_b32_e32 v157, v150
	v_pk_add_f32 v[148:149], v[156:157], v[148:149]
	v_and_b32_e32 v157, 0xffff0000, v92
	v_and_b32_e32 v156, 0xffff0000, v84
	v_mov_b32_e32 v150, v95
	v_pk_add_f32 v[150:151], v[150:151], v[156:157]
	v_lshlrev_b32_e32 v95, 16, v93
	v_lshlrev_b32_e32 v94, 16, v85
	v_mov_b32_e32 v156, v130
	v_mov_b32_e32 v157, v158
	v_pk_add_f32 v[156:157], v[156:157], v[94:95]
	v_and_b32_e32 v92, 0xffff0000, v85
	v_cvt_pk_f32_fp8_e32 v[84:85], v135
	v_cvt_pk_f32_fp8_e32 v[94:95], v134
	v_cvt_pk_f32_fp8_sdwa v[174:175], v135 src0_sel:WORD_1
	v_cvt_pk_f32_fp8_sdwa v[134:135], v134 src0_sel:WORD_1
	v_and_b32_e32 v93, 0xffff0000, v93
	v_mov_b32_e32 v158, v131
	v_pk_add_f32 v[158:159], v[158:159], v[92:93]
	v_lshlrev_b32_e32 v93, 16, v82
	v_lshlrev_b32_e32 v92, 16, v80
	v_mov_b32_e32 v130, v84
	v_mov_b32_e32 v131, v94
	v_pk_add_f32 v[92:93], v[130:131], v[92:93]
	v_and_b32_e32 v131, 0xffff0000, v82
	v_and_b32_e32 v130, 0xffff0000, v80
	v_mov_b32_e32 v94, v85
	v_pk_add_f32 v[94:95], v[94:95], v[130:131]
	v_lshlrev_b32_e32 v85, 16, v83
	v_lshlrev_b32_e32 v84, 16, v81
	v_mov_b32_e32 v130, v174
	v_mov_b32_e32 v131, v134
	v_and_b32_e32 v83, 0xffff0000, v83
	v_and_b32_e32 v82, 0xffff0000, v81
	v_mov_b32_e32 v134, v175
	v_pk_add_f32 v[130:131], v[130:131], v[84:85]
	v_pk_add_f32 v[134:135], v[134:135], v[82:83]
	v_cvt_pk_f32_fp8_e32 v[82:83], v173
	v_cvt_pk_f32_fp8_e32 v[84:85], v171
	v_cvt_pk_f32_fp8_sdwa v[174:175], v173 src0_sel:WORD_1
	v_cvt_pk_f32_fp8_sdwa v[176:177], v171 src0_sel:WORD_1
	v_lshlrev_b32_e32 v81, 16, v144
	v_lshlrev_b32_e32 v80, 16, v86
	v_mov_b32_e32 v178, v82
	v_mov_b32_e32 v179, v84
	v_pk_add_f32 v[80:81], v[178:179], v[80:81]
	v_and_b32_e32 v179, 0xffff0000, v144
	v_and_b32_e32 v178, 0xffff0000, v86
	v_mov_b32_e32 v84, v83
	v_pk_add_f32 v[82:83], v[84:85], v[178:179]
	v_lshlrev_b32_e32 v85, 16, v145
	v_mov_b32_e32 v179, v176
	v_and_b32_e32 v145, 0xffff0000, v145
	v_and_b32_e32 v144, 0xffff0000, v87
	v_mov_b32_e32 v176, v175
	v_lshlrev_b32_e32 v84, 16, v87
	v_pk_add_f32 v[86:87], v[176:177], v[144:145]
	v_cvt_pk_f32_fp8_e32 v[144:145], v170
	v_mov_b32_e32 v178, v174
	v_cvt_pk_f32_fp8_sdwa v[174:175], v170 src0_sel:WORD_1
	v_lshlrev_b32_e32 v170, 16, v140
	v_and_b32_e32 v171, 0xffff0000, v140
	v_pk_add_f32 v[170:171], v[144:145], v[170:171]
	v_cvt_pk_f32_fp8_sdwa v[144:145], v172 src0_sel:WORD_1
	v_lshlrev_b32_e32 v140, 16, v141
	v_and_b32_e32 v141, 0xffff0000, v141
	v_pk_add_f32 v[174:175], v[174:175], v[140:141]
	v_cvt_pk_f32_fp8_e32 v[140:141], v172
	v_lshlrev_b32_e32 v172, 16, v138
	v_and_b32_e32 v173, 0xffff0000, v138
	v_lshlrev_b32_e32 v138, 16, v139
	v_and_b32_e32 v139, 0xffff0000, v139
	v_pk_add_f32 v[182:183], v[144:145], v[138:139]
	v_cvt_pk_f32_fp8_e32 v[138:139], v169
	v_cvt_pk_f32_fp8_e32 v[144:145], v168
	v_pk_add_f32 v[84:85], v[178:179], v[84:85]
	v_pk_add_f32 v[180:181], v[140:141], v[172:173]
	v_cvt_pk_f32_fp8_sdwa v[140:141], v169 src0_sel:WORD_1
	v_cvt_pk_f32_fp8_sdwa v[178:179], v168 src0_sel:WORD_1
	v_lshlrev_b32_e32 v169, 16, v136
	v_lshlrev_b32_e32 v168, 16, v128
	v_mov_b32_e32 v172, v138
	v_mov_b32_e32 v173, v144
	v_pk_add_f32 v[168:169], v[172:173], v[168:169]
	v_and_b32_e32 v173, 0xffff0000, v136
	v_and_b32_e32 v172, 0xffff0000, v128
	v_mov_b32_e32 v144, v139
	v_pk_add_f32 v[172:173], v[144:145], v[172:173]
	v_lshlrev_b32_e32 v139, 16, v137
	v_lshlrev_b32_e32 v138, 16, v129
	v_mov_b32_e32 v144, v140
	v_mov_b32_e32 v145, v178
	v_pk_add_f32 v[176:177], v[144:145], v[138:139]
	v_and_b32_e32 v136, 0xffff0000, v129
	v_cvt_pk_f32_fp8_e32 v[128:129], v166
	v_cvt_pk_f32_fp8_e32 v[138:139], v160
	v_cvt_pk_f32_fp8_sdwa v[144:145], v166 src0_sel:WORD_1
	v_cvt_pk_f32_fp8_sdwa v[184:185], v160 src0_sel:WORD_1
	v_and_b32_e32 v137, 0xffff0000, v137
	v_mov_b32_e32 v178, v141
	v_pk_add_f32 v[178:179], v[178:179], v[136:137]
	v_lshlrev_b32_e32 v137, 16, v90
	v_lshlrev_b32_e32 v136, 16, v88
	v_mov_b32_e32 v140, v128
	v_mov_b32_e32 v141, v138
	v_pk_add_f32 v[136:137], v[140:141], v[136:137]
	v_and_b32_e32 v141, 0xffff0000, v90
	v_and_b32_e32 v140, 0xffff0000, v88
	v_mov_b32_e32 v138, v129
	v_pk_add_f32 v[138:139], v[138:139], v[140:141]
	v_lshlrev_b32_e32 v129, 16, v91
	v_lshlrev_b32_e32 v128, 16, v89
	v_mov_b32_e32 v140, v144
	v_mov_b32_e32 v141, v184
	v_and_b32_e32 v91, 0xffff0000, v91
	v_and_b32_e32 v90, 0xffff0000, v89
	v_mov_b32_e32 v184, v145
	v_pk_add_f32 v[140:141], v[140:141], v[128:129]
	v_pk_add_f32 v[144:145], v[184:185], v[90:91]
	v_cvt_pk_f32_fp8_e32 v[90:91], v155
	v_cvt_pk_f32_fp8_e32 v[128:129], v154
	v_lshlrev_b32_e32 v89, 16, v142
	v_lshlrev_b32_e32 v88, 16, v132
	v_mov_b32_e32 v186, v90
	v_mov_b32_e32 v187, v128
	v_pk_mul_f32 v[228:229], v[146:147], v[146:147]
	v_pk_mul_f32 v[232:233], v[162:163], v[162:163]
	v_pk_add_f32 v[88:89], v[186:187], v[88:89]
	v_and_b32_e32 v187, 0xffff0000, v142
	v_and_b32_e32 v186, 0xffff0000, v132
	v_pk_mul_f32 v[230:231], v[152:153], v[152:153]
	v_pk_mul_f32 v[234:235], v[164:165], v[164:165]
	v_pk_mul_f32 v[236:237], v[150:151], v[150:151]
	v_add_f32_e32 v132, v232, v233
	v_add_f32_e32 v142, v228, v229
	v_pk_fma_f32 v[236:237], v[148:149], v[148:149], v[236:237]
	v_add_f32_e32 v132, v234, v132
	v_add_f32_e32 v142, v230, v142
	v_pk_fma_f32 v[236:237], v[156:157], v[156:157], v[236:237]
	v_pk_mul_f32 v[238:239], v[94:95], v[94:95]
	v_add_f32_e32 v132, v235, v132
	v_add_f32_e32 v142, v231, v142
	v_pk_fma_f32 v[236:237], v[158:159], v[158:159], v[236:237]
	v_pk_fma_f32 v[238:239], v[92:93], v[92:93], v[238:239]
	v_add_f32_e32 v132, v142, v132
	v_pk_fma_f32 v[238:239], v[130:131], v[130:131], v[238:239]
	v_pk_mul_f32 v[240:241], v[82:83], v[82:83]
	v_add_f32_e32 v132, v132, v236
	v_pk_fma_f32 v[238:239], v[134:135], v[134:135], v[238:239]
	v_pk_fma_f32 v[240:241], v[80:81], v[80:81], v[240:241]
	v_add_f32_e32 v132, v132, v237
	v_pk_fma_f32 v[240:241], v[84:85], v[84:85], v[240:241]
	v_add_f32_e32 v132, v132, v238
	v_pk_fma_f32 v[240:241], v[86:87], v[86:87], v[240:241]
	v_add_f32_e32 v132, v132, v239
	v_add_f32_e32 v132, v132, v240
	v_add_f32_e32 v132, v132, v241
	v_cvt_pk_f32_fp8_sdwa v[184:185], v155 src0_sel:WORD_1
	v_cvt_pk_f32_fp8_sdwa v[154:155], v154 src0_sel:WORD_1
	v_add_f32_dpp v132, v132, v132 quad_perm:[1,0,3,2] row_mask:0xf bank_mask:0xf bound_ctrl:1
	v_mov_b32_e32 v128, v91
	v_pk_add_f32 v[90:91], v[128:129], v[186:187]
	v_add_f32_dpp v132, v132, v132 quad_perm:[2,3,0,1] row_mask:0xf bank_mask:0xf bound_ctrl:1
	v_mov_b32_e32 v187, v154
	v_mov_b32_e32 v186, v184
	v_add_f32_dpp v132, v132, v132 row_half_mirror row_mask:0xf bank_mask:0xf bound_ctrl:1
	v_lshlrev_b64 v[234:235], 2, v[78:79]
	v_lshlrev_b32_e32 v129, 16, v143
	v_add_f32_dpp v132, v132, v132 row_mirror row_mask:0xf bank_mask:0xf bound_ctrl:1
	v_lshlrev_b32_e32 v128, 16, v133
	v_readlane_b32 s8, v132, 16
	v_readlane_b32 s9, v132, 48
	v_readlane_b32 s6, v132, 0
	v_readlane_b32 s7, v132, 32
	v_mov_b32_e32 v228, s8
	v_mov_b32_e32 v229, s9
	v_pk_add_f32 v[228:229], s[6:7], v[228:229]
	v_pk_add_f32 v[128:129], v[186:187], v[128:129]
	v_add_f32_e32 v132, v228, v229
	v_fmamk_f32 v132, v132, 0x3a000000, v206
	v_mul_f32_e32 v142, 0x4f800000, v132
	v_cmp_gt_f32_e32 vcc, s49, v132
	v_and_b32_e32 v143, 0xffff0000, v143
	v_pk_mul_f32 v[228:229], v[180:181], v[180:181]
	v_cndmask_b32_e32 v132, v132, v142, vcc
	v_sqrt_f32_e32 v142, v132
	v_pk_mul_f32 v[238:239], v[182:183], v[182:183]
	v_add_f32_e32 v228, v228, v229
	v_add_f32_e32 v228, v238, v228
	v_add_u32_e32 v154, -1, v142
	v_fma_f32 v160, -v154, v142, v132
	v_cmp_ge_f32_e64 s[6:7], 0, v160
	v_add_u32_e32 v160, 1, v142
	v_pk_mul_f32 v[242:243], v[138:139], v[138:139]
	v_cndmask_b32_e64 v154, v142, v154, s[6:7]
	v_fma_f32 v142, -v160, v142, v132
	v_cmp_lt_f32_e64 s[6:7], 0, v142
	v_add_f32_e32 v228, v239, v228
	v_pk_fma_f32 v[242:243], v[136:137], v[136:137], v[242:243]
	v_cndmask_b32_e64 v142, v154, v160, s[6:7]
	v_mul_f32_e32 v154, 0x37800000, v142
	v_cndmask_b32_e32 v142, v142, v154, vcc
	v_cmp_class_f32_e32 vcc, v132, v207
	v_mov_b32_e32 v154, v185
	v_pk_mul_f32 v[184:185], v[172:173], v[172:173]
	v_cndmask_b32_e32 v160, v142, v132, vcc
	v_div_scale_f32 v166, s[6:7], v160, v160, 1.0
	s_ashr_i32 s6, s18, 12
	s_add_i32 s6, s6, 4
	s_mul_hi_i32 s7, s6, 0xc000
	s_mul_i32 s6, s6, 0xc000
	s_add_u32 s6, s2, s6
	s_addc_u32 s7, s3, s7
	s_add_u32 s10, s6, 0xe000
	s_addc_u32 s11, s7, 0
	v_pk_fma_f32 v[230:231], v[168:169], v[168:169], v[184:185]
	s_add_u32 s12, s6, 0x10000
	s_addc_u32 s13, s7, 0
	v_pk_fma_f32 v[230:231], v[176:177], v[176:177], v[230:231]
	v_lshl_add_u64 v[184:185], s[12:13], 0, v[234:235]
	v_pk_fma_f32 v[240:241], v[178:179], v[178:179], v[230:231]
	v_lshl_add_u64 v[230:231], s[22:23], 0, v[234:235]
	v_lshlrev_b32_e32 v250, 4, v189
	v_add_u32_e32 v251, 0x1000, v250
	global_load_dwordx4 v[96:99], v250, s[12:13]
	global_load_dwordx4 v[100:103], v250, s[22:23]
	global_load_dwordx4 v[104:107], v250, s[10:11]
	global_load_dwordx4 v[108:111], v250, s[12:13] offset:1024
	global_load_dwordx4 v[112:115], v250, s[22:23] offset:1024
	global_load_dwordx4 v[116:119], v250, s[10:11] offset:1024
	global_load_dwordx4 v[120:123], v250, s[12:13] offset:2048
	global_load_dwordx4 v[124:127], v250, s[22:23] offset:2048
	global_load_dwordx4 v[212:215], v250, s[10:11] offset:2048
	global_load_dwordx4 v[216:219], v250, s[12:13] offset:3072
	global_load_dwordx4 v[220:223], v250, s[22:23] offset:3072
	global_load_dwordx4 v[224:227], v250, s[10:11] offset:3072
	v_lshl_add_u64 v[234:235], s[10:11], 0, v[234:235]
	v_rcp_f32_e32 v246, v166
	v_and_b32_e32 v142, 0xffff0000, v133
	v_pk_add_f32 v[132:133], v[154:155], v[142:143]
	v_fma_f32 v142, -v166, v246, 1.0
	v_fmac_f32_e32 v246, v142, v246
	v_pk_mul_f32 v[142:143], v[170:171], v[170:171]
	v_pk_mul_f32 v[154:155], v[174:175], v[174:175]
	v_add_f32_e32 v142, v142, v143
	v_add_f32_e32 v142, v154, v142
	v_add_f32_e32 v142, v155, v142
	v_add_f32_e32 v142, v142, v228
	v_pk_fma_f32 v[242:243], v[140:141], v[140:141], v[242:243]
	v_pk_mul_f32 v[244:245], v[90:91], v[90:91]
	v_add_f32_e32 v142, v142, v240
	v_pk_fma_f32 v[242:243], v[144:145], v[144:145], v[242:243]
	v_pk_fma_f32 v[244:245], v[88:89], v[88:89], v[244:245]
	v_add_f32_e32 v142, v142, v241
	v_pk_fma_f32 v[244:245], v[128:129], v[128:129], v[244:245]
	v_add_f32_e32 v142, v142, v242
	v_pk_fma_f32 v[244:245], v[132:133], v[132:133], v[244:245]
	v_add_f32_e32 v142, v142, v243
	v_add_f32_e32 v142, v142, v244
	v_add_f32_e32 v142, v142, v245
	v_div_scale_f32 v247, vcc, 1.0, v160, 1.0
	s_nop 0
	v_add_f32_dpp v142, v142, v142 quad_perm:[1,0,3,2] row_mask:0xf bank_mask:0xf bound_ctrl:1
	v_mul_f32_e32 v248, v247, v246
	v_fma_f32 v154, -v166, v248, v247
	v_add_f32_dpp v142, v142, v142 quad_perm:[2,3,0,1] row_mask:0xf bank_mask:0xf bound_ctrl:1
	v_fmac_f32_e32 v248, v154, v246
	v_fma_f32 v154, -v166, v248, v247
	v_add_f32_dpp v142, v142, v142 row_half_mirror row_mask:0xf bank_mask:0xf bound_ctrl:1
	v_div_fmas_f32 v154, v154, v246, v248
	v_lshrrev_b32_e32 v229, 1, v189
	v_add_f32_dpp v142, v142, v142 row_mirror row_mask:0xf bank_mask:0xf bound_ctrl:1
	v_add_u32_e32 v246, 64, v229
	v_readlane_b32 s8, v142, 16
	v_readlane_b32 s9, v142, 48
	v_readlane_b32 s6, v142, 0
	v_readlane_b32 s7, v142, 32
	v_mov_b32_e32 v142, s8
	v_mov_b32_e32 v143, s9
	v_pk_add_f32 v[142:143], s[6:7], v[142:143]
	s_ashr_i32 s19, s18, 31
	v_add_f32_e32 v142, v142, v143
	v_fmamk_f32 v142, v142, 0x3a000000, v206
	v_mul_f32_e32 v143, 0x4f800000, v142
	v_cmp_gt_f32_e64 s[6:7], s49, v142
	s_waitcnt vmcnt(11)
	v_pk_add_f32 v[96:97], v[96:97], 1.0 op_sel_hi:[1,0]
	v_cndmask_b32_e64 v142, v142, v143, s[6:7]
	v_sqrt_f32_e32 v143, v142
	s_nop 0
	v_add_u32_e32 v155, -1, v143
	v_fma_f32 v166, -v155, v143, v142
	v_cmp_ge_f32_e64 s[8:9], 0, v166
	v_add_u32_e32 v166, 1, v143
	s_nop 0
	v_cndmask_b32_e64 v155, v143, v155, s[8:9]
	v_fma_f32 v143, -v166, v143, v142
	v_cmp_lt_f32_e64 s[8:9], 0, v143
	s_nop 1
	v_cndmask_b32_e64 v143, v155, v166, s[8:9]
	v_mul_f32_e32 v155, 0x37800000, v143
	v_cndmask_b32_e64 v143, v143, v155, s[6:7]
	v_cmp_class_f32_e64 s[6:7], v142, v207
	v_div_fixup_f32 v166, v154, v160, 1.0
	v_pk_mul_f32 v[146:147], v[146:147], v[166:167] op_sel_hi:[1,0]
	v_cndmask_b32_e64 v142, v143, v142, s[6:7]
	v_div_scale_f32 v143, s[6:7], v142, v142, 1.0
	v_rcp_f32_e32 v155, v143
	s_waitcnt vmcnt(10)
	v_pk_mul_f32 v[146:147], v[100:101], v[146:147]
	v_pk_mul_f32 v[152:153], v[152:153], v[166:167] op_sel_hi:[1,0]
	v_pk_mul_f32 v[164:165], v[164:165], v[166:167] op_sel_hi:[1,0]
	v_fma_f32 v154, -v143, v155, 1.0
	v_fmac_f32_e32 v155, v154, v155
	v_div_scale_f32 v154, vcc, 1.0, v142, 1.0
	v_mul_f32_e32 v160, v154, v155
	v_fma_f32 v228, -v143, v160, v154
	v_fmac_f32_e32 v160, v228, v155
	v_fma_f32 v143, -v143, v160, v154
	v_div_fmas_f32 v143, v143, v155, v160
	v_div_fixup_f32 v160, v143, v142, 1.0
	v_lshlrev_b32_e32 v142, 3, v189
	v_and_b32_e32 v228, 8, v142
	v_pk_add_f32 v[142:143], v[98:99], 1.0 op_sel_hi:[1,0]
	s_waitcnt vmcnt(9)
	v_pk_fma_f32 v[154:155], v[96:97], v[146:147], v[104:105]
	v_pk_mul_f32 v[152:153], v[102:103], v[152:153]
	v_cvt_pk_bf16_f32 v146, v154, v155
	v_pk_mul_f32 v[170:171], v[170:171], v[160:161] op_sel_hi:[1,0]
	v_lshlrev_b32_e32 v186, 16, v146
	v_and_b32_e32 v187, 0xffff0000, v146
	v_sub_f32_e32 v186, v154, v186
	v_sub_f32_e32 v187, v155, v187
	v_pk_fma_f32 v[152:153], v[142:143], v[152:153], v[106:107]
	v_pk_mul_f32 v[170:171], v[100:101], v[170:171]
	v_cvt_pk_bf16_f32 v147, v152, v153
	v_cvt_pk_bf16_f32 v186, v186, v187
	v_pk_mul_f32 v[162:163], v[162:163], v[166:167] op_sel_hi:[1,0]
	v_lshlrev_b32_e32 v187, 16, v147
	v_and_b32_e32 v238, 0xffff0000, v147
	v_sub_f32_e32 v187, v152, v187
	v_sub_f32_e32 v238, v153, v238
	v_cvt_pk_bf16_f32 v187, v187, v238
	v_xor_b32_e32 v238, s43, v229
	v_lshlrev_b32_e32 v238, 4, v238
	v_add3_u32 v238, s44, v238, v228
	ds_write_b64 v238, v[146:147]
	v_add_u32_e32 v146, 0x10000, v238
	ds_write_b64 v146, v[186:187]
	v_pk_mul_f32 v[146:147], v[174:175], v[160:161] op_sel_hi:[1,0]
	v_xor_b32_e32 v238, s45, v229
	v_pk_mul_f32 v[146:147], v[102:103], v[146:147]
	v_lshlrev_b32_e32 v238, 4, v238
	v_pk_fma_f32 v[142:143], v[142:143], v[146:147], v[106:107]
	v_pk_fma_f32 v[146:147], v[96:97], v[170:171], v[104:105]
	v_lshlrev_b64 v[234:235], 2, v[76:77]
	v_cvt_pk_bf16_f32 v170, v146, v147
	v_cvt_pk_bf16_f32 v171, v142, v143
	v_lshl_add_u64 v[230:231], s[22:23], 0, v[234:235]
	v_lshlrev_b32_e32 v174, 16, v170
	v_and_b32_e32 v175, 0xffff0000, v170
	v_sub_f32_e32 v174, v146, v174
	v_sub_f32_e32 v175, v147, v175
	v_cvt_pk_bf16_f32 v174, v174, v175
	v_lshlrev_b32_e32 v175, 16, v171
	v_and_b32_e32 v184, 0xffff0000, v171
	v_sub_f32_e32 v175, v142, v175
	v_sub_f32_e32 v184, v143, v184
	v_cvt_pk_bf16_f32 v175, v175, v184
	v_lshl_add_u64 v[184:185], s[12:13], 0, v[234:235]
	v_lshl_add_u64 v[234:235], s[10:11], 0, v[234:235]
	v_add3_u32 v238, s46, v238, v228
	ds_write_b64 v238, v[170:171]
	v_add_u32_e32 v170, 0x10000, v238
	ds_write_b64 v170, v[174:175]
	v_add_u32_e32 v238, 32, v229
	s_lshl_b64 s[6:7], s[18:19], 11
	s_add_u32 s6, s41, s6
	s_addc_u32 s7, s42, s7
	s_waitcnt vmcnt(8)
	v_pk_add_f32 v[110:111], v[110:111], 1.0 op_sel_hi:[1,0]
	v_pk_add_f32 v[108:109], v[108:109], 1.0 op_sel_hi:[1,0]
	s_waitcnt vmcnt(7)
	v_pk_mul_f32 v[162:163], v[162:163], v[112:113]
	v_pk_mul_f32 v[164:165], v[164:165], v[114:115]
	s_waitcnt vmcnt(6)
	v_pk_fma_f32 v[174:175], v[162:163], v[108:109], v[116:117]
	v_pk_fma_f32 v[170:171], v[164:165], v[110:111], v[118:119]
	v_cvt_pk_bf16_f32 v162, v174, v175
	s_nop 0
	v_lshlrev_b32_e32 v164, 16, v162
	v_and_b32_e32 v165, 0xffff0000, v162
	v_sub_f32_e32 v164, v174, v164
	v_sub_f32_e32 v165, v175, v165
	v_cvt_pk_bf16_f32 v163, v170, v171
	v_cvt_pk_bf16_f32 v164, v164, v165
	s_nop 0
	v_lshlrev_b32_e32 v165, 16, v163
	v_and_b32_e32 v239, 0xffff0000, v163
	v_sub_f32_e32 v165, v170, v165
	v_sub_f32_e32 v239, v171, v239
	v_cvt_pk_bf16_f32 v165, v165, v239
	v_xor_b32_e32 v239, s43, v238
	v_lshlrev_b32_e32 v239, 4, v239
	v_add3_u32 v239, s44, v239, v228
	ds_write_b64 v239, v[162:163]
	v_add_u32_e32 v162, 0x10000, v239
	ds_write_b64 v162, v[164:165]
	v_pk_mul_f32 v[164:165], v[180:181], v[160:161] op_sel_hi:[1,0]
	v_pk_mul_f32 v[162:163], v[182:183], v[160:161] op_sel_hi:[1,0]
	v_pk_mul_f32 v[164:165], v[164:165], v[112:113]
	v_pk_mul_f32 v[162:163], v[162:163], v[114:115]
	v_pk_fma_f32 v[164:165], v[164:165], v[108:109], v[116:117]
	v_pk_fma_f32 v[162:163], v[162:163], v[110:111], v[118:119]
	v_cvt_pk_bf16_f32 v184, v164, v165
	v_lshlrev_b64 v[234:235], 2, v[74:75]
	v_lshlrev_b32_e32 v180, 16, v184
	v_and_b32_e32 v181, 0xffff0000, v184
	v_sub_f32_e32 v180, v164, v180
	v_sub_f32_e32 v181, v165, v181
	v_cvt_pk_bf16_f32 v185, v162, v163
	v_cvt_pk_bf16_f32 v186, v180, v181
	v_lshl_add_u64 v[230:231], s[22:23], 0, v[234:235]
	v_lshlrev_b32_e32 v180, 16, v185
	v_and_b32_e32 v181, 0xffff0000, v185
	v_sub_f32_e32 v180, v162, v180
	v_sub_f32_e32 v181, v163, v181
	v_cvt_pk_bf16_f32 v187, v180, v181
	v_lshl_add_u64 v[180:181], s[12:13], 0, v[234:235]
	v_lshl_add_u64 v[234:235], s[10:11], 0, v[234:235]
	v_xor_b32_e32 v238, s45, v238
	v_lshlrev_b32_e32 v238, 4, v238
	v_add3_u32 v238, s46, v238, v228
	ds_write_b64 v238, v[184:185]
	v_add_u32_e32 v184, 0x10000, v238
	ds_write_b64 v184, v[186:187]
	v_mov_b32_e32 v184, v148
	v_mov_b32_e32 v185, v150
	v_pk_mul_f32 v[184:185], v[184:185], v[166:167] op_sel_hi:[1,0]
	s_waitcnt vmcnt(5)
	v_pk_add_f32 v[238:239], v[120:121], 1.0 op_sel_hi:[1,0]
	v_mov_b32_e32 v180, v156
	v_mov_b32_e32 v181, v158
	v_pk_mul_f32 v[180:181], v[180:181], v[166:167] op_sel_hi:[1,0]
	v_pk_add_f32 v[122:123], v[122:123], 1.0 op_sel_hi:[1,0]
	s_waitcnt vmcnt(4)
	v_pk_mul_f32 v[186:187], v[184:185], v[124:125]
	v_pk_mul_f32 v[180:181], v[180:181], v[126:127]
	s_waitcnt vmcnt(3)
	v_pk_fma_f32 v[186:187], v[186:187], v[238:239], v[212:213]
	v_pk_fma_f32 v[184:185], v[180:181], v[122:123], v[214:215]
	v_cvt_pk_bf16_f32 v180, v186, v187
	v_mov_b32_e32 v158, v157
	v_lshlrev_b32_e32 v148, 16, v180
	v_sub_f32_e32 v148, v186, v148
	v_and_b32_e32 v150, 0xffff0000, v180
	v_cvt_pk_bf16_f32 v181, v184, v185
	v_sub_f32_e32 v150, v187, v150
	v_cvt_pk_bf16_f32 v240, v148, v150
	v_lshlrev_b32_e32 v148, 16, v181
	v_sub_f32_e32 v148, v184, v148
	v_and_b32_e32 v150, 0xffff0000, v181
	v_sub_f32_e32 v150, v185, v150
	v_cvt_pk_bf16_f32 v241, v148, v150
	v_xor_b32_e32 v148, s43, v246
	v_lshlrev_b32_e32 v148, 4, v148
	v_add3_u32 v148, s44, v148, v228
	ds_write_b64 v148, v[180:181]
	v_add_u32_e32 v148, 0x10000, v148
	ds_write_b64 v148, v[240:241]
	v_mov_b32_e32 v180, v176
	v_mov_b32_e32 v181, v178
	v_mov_b32_e32 v240, v168
	v_mov_b32_e32 v241, v172
	v_pk_mul_f32 v[180:181], v[180:181], v[160:161] op_sel_hi:[1,0]
	v_pk_mul_f32 v[240:241], v[240:241], v[160:161] op_sel_hi:[1,0]
	v_pk_mul_f32 v[180:181], v[180:181], v[126:127]
	v_pk_mul_f32 v[124:125], v[240:241], v[124:125]
	v_pk_fma_f32 v[180:181], v[180:181], v[122:123], v[214:215]
	v_pk_fma_f32 v[182:183], v[124:125], v[238:239], v[212:213]
	v_lshlrev_b64 v[238:239], 2, v[72:73]
	v_cvt_pk_bf16_f32 v242, v182, v183
	v_cvt_pk_bf16_f32 v243, v180, v181
	v_lshl_add_u64 v[230:231], s[12:13], 0, v[238:239]
	v_lshlrev_b32_e32 v148, 16, v242
	v_and_b32_e32 v150, 0xffff0000, v242
	v_sub_f32_e32 v148, v182, v148
	v_sub_f32_e32 v150, v183, v150
	v_cvt_pk_bf16_f32 v244, v148, v150
	v_lshlrev_b32_e32 v148, 16, v243
	v_and_b32_e32 v150, 0xffff0000, v243
	v_lshl_add_u64 v[234:235], s[22:23], 0, v[238:239]
	v_sub_f32_e32 v148, v180, v148
	v_sub_f32_e32 v150, v181, v150
	v_cvt_pk_bf16_f32 v245, v148, v150
	v_lshl_add_u64 v[238:239], s[10:11], 0, v[238:239]
	v_xor_b32_e32 v148, s45, v246
	v_lshlrev_b32_e32 v148, 4, v148
	v_add3_u32 v148, s46, v148, v228
	ds_write_b64 v148, v[242:243]
	v_add_u32_e32 v148, 0x10000, v148
	v_mov_b32_e32 v150, v149
	ds_write_b64 v148, v[244:245]
	v_pk_mul_f32 v[156:157], v[158:159], v[166:167] op_sel_hi:[1,0]
	v_pk_mul_f32 v[148:149], v[150:151], v[166:167] op_sel_hi:[1,0]
	v_add_u32_e32 v242, 0x60, v229
	v_mov_b32_e32 v172, v169
	v_mov_b32_e32 v178, v177
	v_add_u32_e32 v246, 0x80, v229
	s_waitcnt vmcnt(2)
	v_pk_add_f32 v[218:219], v[218:219], 1.0 op_sel_hi:[1,0]
	v_pk_add_f32 v[216:217], v[216:217], 1.0 op_sel_hi:[1,0]
	s_waitcnt vmcnt(1)
	v_pk_mul_f32 v[148:149], v[148:149], v[220:221]
	v_pk_mul_f32 v[150:151], v[156:157], v[222:223]
	s_waitcnt vmcnt(0)
	v_pk_fma_f32 v[158:159], v[148:149], v[216:217], v[224:225]
	v_pk_fma_f32 v[156:157], v[150:151], v[218:219], v[226:227]
	v_cvt_pk_bf16_f32 v148, v158, v159
	s_nop 0
	v_lshlrev_b32_e32 v150, 16, v148
	v_and_b32_e32 v151, 0xffff0000, v148
	v_sub_f32_e32 v150, v158, v150
	v_sub_f32_e32 v151, v159, v151
	v_cvt_pk_bf16_f32 v149, v156, v157
	v_cvt_pk_bf16_f32 v150, v150, v151
	s_nop 0
	v_lshlrev_b32_e32 v151, 16, v149
	v_and_b32_e32 v168, 0xffff0000, v149
	v_sub_f32_e32 v151, v156, v151
	v_sub_f32_e32 v168, v157, v168
	v_cvt_pk_bf16_f32 v151, v151, v168
	v_xor_b32_e32 v168, s43, v242
	v_lshlrev_b32_e32 v168, 4, v168
	v_add3_u32 v168, s44, v168, v228
	ds_write_b64 v168, v[148:149]
	v_add_u32_e32 v148, 0x10000, v168
	ds_write_b64 v148, v[150:151]
	v_pk_mul_f32 v[150:151], v[172:173], v[160:161] op_sel_hi:[1,0]
	v_pk_mul_f32 v[148:149], v[178:179], v[160:161] op_sel_hi:[1,0]
	v_pk_mul_f32 v[150:151], v[150:151], v[220:221]
	v_pk_mul_f32 v[148:149], v[148:149], v[222:223]
	v_pk_fma_f32 v[150:151], v[150:151], v[216:217], v[224:225]
	v_pk_fma_f32 v[148:149], v[148:149], v[218:219], v[226:227]
	v_cvt_pk_bf16_f32 v168, v150, v151
	v_lshlrev_b64 v[234:235], 2, v[70:71]
	v_lshlrev_b32_e32 v172, 16, v168
	v_and_b32_e32 v173, 0xffff0000, v168
	v_sub_f32_e32 v172, v150, v172
	v_sub_f32_e32 v173, v151, v173
	v_cvt_pk_bf16_f32 v169, v148, v149
	v_cvt_pk_bf16_f32 v172, v172, v173
	v_lshl_add_u64 v[230:231], s[22:23], 0, v[234:235]
	v_lshlrev_b32_e32 v173, 16, v169
	v_and_b32_e32 v176, 0xffff0000, v169
	v_sub_f32_e32 v173, v148, v173
	v_sub_f32_e32 v176, v149, v176
	v_cvt_pk_bf16_f32 v173, v173, v176
	v_lshl_add_u64 v[176:177], s[12:13], 0, v[234:235]
	global_load_dwordx4 v[96:99], v251, s[12:13]
	global_load_dwordx4 v[100:103], v251, s[22:23]
	global_load_dwordx4 v[104:107], v251, s[10:11]
	global_load_dwordx4 v[108:111], v251, s[12:13] offset:1024
	global_load_dwordx4 v[112:115], v251, s[22:23] offset:1024
	global_load_dwordx4 v[116:119], v251, s[10:11] offset:1024
	global_load_dwordx4 v[120:123], v251, s[12:13] offset:2048
	global_load_dwordx4 v[124:127], v251, s[22:23] offset:2048
	global_load_dwordx4 v[212:215], v251, s[10:11] offset:2048
	global_load_dwordx4 v[216:219], v251, s[12:13] offset:3072
	global_load_dwordx4 v[220:223], v251, s[22:23] offset:3072
	global_load_dwordx4 v[224:227], v251, s[10:11] offset:3072
	v_lshl_add_u64 v[234:235], s[10:11], 0, v[234:235]
	v_xor_b32_e32 v238, s45, v242
	v_lshlrev_b32_e32 v238, 4, v238
	v_add3_u32 v238, s46, v238, v228
	ds_write_b64 v238, v[168:169]
	v_add_u32_e32 v168, 0x10000, v238
	ds_write_b64 v168, v[172:173]
	s_waitcnt vmcnt(11)
	v_pk_add_f32 v[168:169], v[98:99], 1.0 op_sel_hi:[1,0]
	v_mov_b32_e32 v178, v92
	v_mov_b32_e32 v179, v94
	v_pk_mul_f32 v[178:179], v[178:179], v[166:167] op_sel_hi:[1,0]
	v_pk_add_f32 v[172:173], v[96:97], 1.0 op_sel_hi:[1,0]
	v_mov_b32_e32 v176, v130
	v_mov_b32_e32 v177, v134
	s_waitcnt vmcnt(10)
	v_pk_mul_f32 v[178:179], v[178:179], v[100:101]
	v_pk_mul_f32 v[176:177], v[176:177], v[166:167] op_sel_hi:[1,0]
	s_waitcnt vmcnt(9)
	v_pk_fma_f32 v[178:179], v[178:179], v[172:173], v[104:105]
	v_pk_mul_f32 v[176:177], v[176:177], v[102:103]
	v_cvt_pk_bf16_f32 v238, v178, v179
	v_mov_b32_e32 v134, v131
	v_lshlrev_b32_e32 v92, 16, v238
	v_sub_f32_e32 v92, v178, v92
	v_and_b32_e32 v94, 0xffff0000, v238
	v_pk_fma_f32 v[176:177], v[176:177], v[168:169], v[106:107]
	v_sub_f32_e32 v94, v179, v94
	v_cvt_pk_bf16_f32 v239, v176, v177
	v_cvt_pk_bf16_f32 v240, v92, v94
	v_pk_mul_f32 v[130:131], v[134:135], v[166:167] op_sel_hi:[1,0]
	v_lshlrev_b32_e32 v92, 16, v239
	v_sub_f32_e32 v92, v176, v92
	v_and_b32_e32 v94, 0xffff0000, v239
	v_sub_f32_e32 v94, v177, v94
	v_cvt_pk_bf16_f32 v241, v92, v94
	v_xor_b32_e32 v92, s43, v246
	v_lshlrev_b32_e32 v92, 4, v92
	v_add3_u32 v92, s44, v92, v228
	ds_write_b64 v92, v[238:239]
	v_add_u32_e32 v92, 0x10000, v92
	ds_write_b64 v92, v[240:241]
	v_mov_b32_e32 v240, v136
	v_mov_b32_e32 v241, v138
	v_pk_mul_f32 v[240:241], v[240:241], v[160:161] op_sel_hi:[1,0]
	v_mov_b32_e32 v238, v140
	v_mov_b32_e32 v239, v144
	v_pk_mul_f32 v[100:101], v[240:241], v[100:101]
	v_pk_mul_f32 v[238:239], v[238:239], v[160:161] op_sel_hi:[1,0]
	v_pk_fma_f32 v[172:173], v[100:101], v[172:173], v[104:105]
	v_pk_mul_f32 v[102:103], v[238:239], v[102:103]
	v_cvt_pk_bf16_f32 v242, v172, v173
	v_lshlrev_b64 v[238:239], 2, v[68:69]
	v_lshlrev_b32_e32 v92, 16, v242
	v_and_b32_e32 v94, 0xffff0000, v242
	v_sub_f32_e32 v92, v172, v92
	v_sub_f32_e32 v94, v173, v94
	v_pk_fma_f32 v[168:169], v[102:103], v[168:169], v[106:107]
	v_lshl_add_u64 v[230:231], s[12:13], 0, v[238:239]
	v_cvt_pk_bf16_f32 v243, v168, v169
	v_cvt_pk_bf16_f32 v244, v92, v94
	v_lshl_add_u64 v[234:235], s[22:23], 0, v[238:239]
	v_lshlrev_b32_e32 v92, 16, v243
	v_and_b32_e32 v94, 0xffff0000, v243
	v_sub_f32_e32 v92, v168, v92
	v_sub_f32_e32 v94, v169, v94
	v_cvt_pk_bf16_f32 v245, v92, v94
	v_lshl_add_u64 v[238:239], s[10:11], 0, v[238:239]
	v_xor_b32_e32 v92, s45, v246
	v_lshlrev_b32_e32 v92, 4, v92
	v_add3_u32 v92, s46, v92, v228
	ds_write_b64 v92, v[242:243]
	v_add_u32_e32 v92, 0x10000, v92
	v_mov_b32_e32 v94, v93
	ds_write_b64 v92, v[244:245]
	v_pk_mul_f32 v[92:93], v[94:95], v[166:167] op_sel_hi:[1,0]
	v_add_u32_e32 v242, 0xa0, v229
	v_mov_b32_e32 v138, v137
	v_mov_b32_e32 v144, v141
	v_add_u32_e32 v246, 0xc0, v229
	s_waitcnt vmcnt(8)
	v_pk_add_f32 v[110:111], v[110:111], 1.0 op_sel_hi:[1,0]
	v_pk_add_f32 v[108:109], v[108:109], 1.0 op_sel_hi:[1,0]
	s_waitcnt vmcnt(7)
	v_pk_mul_f32 v[92:93], v[92:93], v[112:113]
	v_pk_mul_f32 v[94:95], v[130:131], v[114:115]
	s_waitcnt vmcnt(6)
	v_pk_fma_f32 v[134:135], v[92:93], v[108:109], v[116:117]
	v_pk_fma_f32 v[130:131], v[94:95], v[110:111], v[118:119]
	v_cvt_pk_bf16_f32 v92, v134, v135
	s_nop 0
	v_lshlrev_b32_e32 v94, 16, v92
	v_and_b32_e32 v95, 0xffff0000, v92
	v_sub_f32_e32 v94, v134, v94
	v_sub_f32_e32 v95, v135, v95
	v_cvt_pk_bf16_f32 v93, v130, v131
	v_cvt_pk_bf16_f32 v94, v94, v95
	s_nop 0
	v_lshlrev_b32_e32 v95, 16, v93
	v_and_b32_e32 v136, 0xffff0000, v93
	v_sub_f32_e32 v95, v130, v95
	v_sub_f32_e32 v136, v131, v136
	v_cvt_pk_bf16_f32 v95, v95, v136
	v_xor_b32_e32 v136, s43, v242
	v_lshlrev_b32_e32 v136, 4, v136
	v_add3_u32 v136, s44, v136, v228
	ds_write_b64 v136, v[92:93]
	v_add_u32_e32 v92, 0x10000, v136
	ds_write_b64 v92, v[94:95]
	v_pk_mul_f32 v[94:95], v[138:139], v[160:161] op_sel_hi:[1,0]
	v_pk_mul_f32 v[92:93], v[144:145], v[160:161] op_sel_hi:[1,0]
	v_pk_mul_f32 v[94:95], v[94:95], v[112:113]
	v_pk_mul_f32 v[92:93], v[92:93], v[114:115]
	v_pk_fma_f32 v[94:95], v[94:95], v[108:109], v[116:117]
	v_pk_fma_f32 v[92:93], v[92:93], v[110:111], v[118:119]
	v_cvt_pk_bf16_f32 v140, v94, v95
	v_lshlrev_b64 v[234:235], 2, v[66:67]
	v_lshlrev_b32_e32 v136, 16, v140
	v_and_b32_e32 v137, 0xffff0000, v140
	v_sub_f32_e32 v136, v94, v136
	v_sub_f32_e32 v137, v95, v137
	v_cvt_pk_bf16_f32 v141, v92, v93
	v_cvt_pk_bf16_f32 v144, v136, v137
	v_lshl_add_u64 v[230:231], s[22:23], 0, v[234:235]
	v_lshlrev_b32_e32 v136, 16, v141
	v_and_b32_e32 v137, 0xffff0000, v141
	v_sub_f32_e32 v136, v92, v136
	v_sub_f32_e32 v137, v93, v137
	v_cvt_pk_bf16_f32 v145, v136, v137
	v_lshl_add_u64 v[136:137], s[12:13], 0, v[234:235]
	v_lshl_add_u64 v[234:235], s[10:11], 0, v[234:235]
	v_xor_b32_e32 v238, s45, v242
	v_lshlrev_b32_e32 v238, 4, v238
	v_add3_u32 v238, s46, v238, v228
	ds_write_b64 v238, v[140:141]
	v_add_u32_e32 v140, 0x10000, v238
	ds_write_b64 v140, v[144:145]
	v_mov_b32_e32 v144, v80
	v_mov_b32_e32 v145, v82
	v_pk_mul_f32 v[144:145], v[144:145], v[166:167] op_sel_hi:[1,0]
	s_waitcnt vmcnt(5)
	v_pk_add_f32 v[140:141], v[120:121], 1.0 op_sel_hi:[1,0]
	v_mov_b32_e32 v136, v84
	v_mov_b32_e32 v137, v86
	v_pk_mul_f32 v[136:137], v[136:137], v[166:167] op_sel_hi:[1,0]
	v_pk_add_f32 v[122:123], v[122:123], 1.0 op_sel_hi:[1,0]
	s_waitcnt vmcnt(4)
	v_pk_mul_f32 v[144:145], v[144:145], v[124:125]
	v_pk_mul_f32 v[136:137], v[136:137], v[126:127]
	s_waitcnt vmcnt(3)
	v_pk_fma_f32 v[144:145], v[144:145], v[140:141], v[212:213]
	v_pk_fma_f32 v[242:243], v[136:137], v[122:123], v[214:215]
	v_cvt_pk_bf16_f32 v136, v144, v145
	v_mov_b32_e32 v86, v85
	v_lshlrev_b32_e32 v80, 16, v136
	v_sub_f32_e32 v80, v144, v80
	v_and_b32_e32 v82, 0xffff0000, v136
	v_cvt_pk_bf16_f32 v137, v242, v243
	v_sub_f32_e32 v82, v145, v82
	v_cvt_pk_bf16_f32 v238, v80, v82
	v_lshlrev_b32_e32 v80, 16, v137
	v_sub_f32_e32 v80, v242, v80
	v_and_b32_e32 v82, 0xffff0000, v137
	v_sub_f32_e32 v82, v243, v82
	v_cvt_pk_bf16_f32 v239, v80, v82
	v_xor_b32_e32 v80, s43, v246
	v_lshlrev_b32_e32 v80, 4, v80
	v_add3_u32 v80, s44, v80, v228
	ds_write_b64 v80, v[136:137]
	v_add_u32_e32 v80, 0x10000, v80
	ds_write_b64 v80, v[238:239]
	v_mov_b32_e32 v136, v128
	v_mov_b32_e32 v137, v132
	v_mov_b32_e32 v238, v88
	v_mov_b32_e32 v239, v90
	v_pk_mul_f32 v[136:137], v[136:137], v[160:161] op_sel_hi:[1,0]
	v_pk_mul_f32 v[238:239], v[238:239], v[160:161] op_sel_hi:[1,0]
	v_pk_mul_f32 v[136:137], v[136:137], v[126:127]
	v_pk_mul_f32 v[124:125], v[238:239], v[124:125]
	v_pk_fma_f32 v[136:137], v[136:137], v[122:123], v[214:215]
	v_pk_fma_f32 v[138:139], v[124:125], v[140:141], v[212:213]
	v_lshlrev_b64 v[238:239], 2, v[64:65]
	v_cvt_pk_bf16_f32 v140, v138, v139
	v_cvt_pk_bf16_f32 v141, v136, v137
	v_lshl_add_u64 v[230:231], s[12:13], 0, v[238:239]
	v_lshlrev_b32_e32 v80, 16, v140
	v_and_b32_e32 v82, 0xffff0000, v140
	v_sub_f32_e32 v80, v138, v80
	v_sub_f32_e32 v82, v139, v82
	v_cvt_pk_bf16_f32 v244, v80, v82
	v_lshlrev_b32_e32 v80, 16, v141
	v_and_b32_e32 v82, 0xffff0000, v141
	v_lshl_add_u64 v[234:235], s[22:23], 0, v[238:239]
	v_sub_f32_e32 v80, v136, v80
	v_sub_f32_e32 v82, v137, v82
	v_cvt_pk_bf16_f32 v245, v80, v82
	v_lshl_add_u64 v[238:239], s[10:11], 0, v[238:239]
	v_xor_b32_e32 v80, s45, v246
	v_lshlrev_b32_e32 v80, 4, v80
	v_add3_u32 v80, s46, v80, v228
	ds_write_b64 v80, v[140:141]
	v_add_u32_e32 v80, 0x10000, v80
	v_mov_b32_e32 v82, v81
	ds_write_b64 v80, v[244:245]
	v_pk_mul_f32 v[80:81], v[82:83], v[166:167] op_sel_hi:[1,0]
	v_pk_mul_f32 v[84:85], v[86:87], v[166:167] op_sel_hi:[1,0]
	v_add_u32_e32 v128, 0xe0, v229
	v_mov_b32_e32 v90, v89
	v_mov_b32_e32 v132, v129
	s_waitcnt vmcnt(2)
	v_pk_add_f32 v[216:217], v[216:217], 1.0 op_sel_hi:[1,0]
	v_pk_add_f32 v[140:141], v[218:219], 1.0 op_sel_hi:[1,0]
	s_waitcnt vmcnt(1)
	v_pk_mul_f32 v[80:81], v[80:81], v[220:221]
	v_pk_mul_f32 v[82:83], v[84:85], v[222:223]
	s_waitcnt vmcnt(0)
	v_pk_fma_f32 v[80:81], v[80:81], v[216:217], v[224:225]
	v_pk_fma_f32 v[82:83], v[82:83], v[140:141], v[226:227]
	v_cvt_pk_bf16_f32 v84, v80, v81
	s_nop 0
	v_lshlrev_b32_e32 v86, 16, v84
	v_and_b32_e32 v87, 0xffff0000, v84
	v_sub_f32_e32 v86, v80, v86
	v_sub_f32_e32 v87, v81, v87
	v_cvt_pk_bf16_f32 v85, v82, v83
	v_cvt_pk_bf16_f32 v86, v86, v87
	s_nop 0
	v_lshlrev_b32_e32 v87, 16, v85
	v_and_b32_e32 v88, 0xffff0000, v85
	v_sub_f32_e32 v87, v82, v87
	v_sub_f32_e32 v88, v83, v88
	v_cvt_pk_bf16_f32 v87, v87, v88
	v_xor_b32_e32 v88, s43, v128
	v_lshlrev_b32_e32 v88, 4, v88
	v_add3_u32 v88, s44, v88, v228
	ds_write_b64 v88, v[84:85]
	v_add_u32_e32 v84, 0x10000, v88
	ds_write_b64 v84, v[86:87]
	v_pk_mul_f32 v[86:87], v[90:91], v[160:161] op_sel_hi:[1,0]
	v_pk_mul_f32 v[84:85], v[132:133], v[160:161] op_sel_hi:[1,0]
	v_pk_mul_f32 v[86:87], v[86:87], v[220:221]
	v_pk_mul_f32 v[84:85], v[84:85], v[222:223]
	v_pk_fma_f32 v[86:87], v[86:87], v[216:217], v[224:225]
	v_xor_b32_e32 v128, s45, v128
	v_cvt_pk_bf16_f32 v88, v86, v87
	v_pk_fma_f32 v[84:85], v[84:85], v[140:141], v[226:227]
	s_cmp_lt_i32 s56, s39
	s_cbranch_scc0 .Lpf_skip_1
	s_add_i32 s98, s38, s18
	s_ashr_i32 s99, s98, 31
	s_lshl_b64 s[100:101], s[98:99], 11
	s_lshl_b64 s[98:99], s[98:99], 12
	s_add_u32 s98, s35, s98
	s_addc_u32 s99, s36, s99
	s_add_u32 s100, s37, s100
	v_lshlrev_b64 v[112:113], 1, v[78:79]
	s_addc_u32 s101, s40, s101
	v_lshl_add_u64 v[110:111], s[98:99], 0, v[112:113]
	s_add_i32 s98, s47, s18
	s_ashr_i32 s99, s98, 31
	v_lshl_add_u64 v[114:115], s[100:101], 0, v[78:79]
	s_lshl_b64 s[100:101], s[98:99], 11
	s_lshl_b64 s[98:99], s[98:99], 12
	s_add_u32 s98, s35, s98
	s_addc_u32 s99, s36, s99
	s_add_u32 s100, s37, s100
	s_addc_u32 s101, s40, s101
	v_lshl_add_u64 v[126:127], s[98:99], 0, v[112:113]
	global_load_dwordx2 v[96:97], v[110:111], off
	global_load_dwordx2 v[98:99], v[110:111], off offset:512
	global_load_dwordx2 v[100:101], v[110:111], off offset:1024
	global_load_dwordx2 v[102:103], v[110:111], off offset:1536
	global_load_dwordx2 v[104:105], v[110:111], off offset:2048
	global_load_dwordx2 v[106:107], v[110:111], off offset:2560
	global_load_dwordx2 v[108:109], v[110:111], off offset:3072
	s_nop 0
	global_load_dwordx2 v[110:111], v[110:111], off offset:3584
	s_nop 0
	global_load_dword v212, v[114:115], off
	global_load_dword v213, v[114:115], off offset:256
	global_load_dword v214, v[114:115], off offset:512
	global_load_dword v215, v[114:115], off offset:768
	global_load_dword v216, v[114:115], off offset:1024
	global_load_dword v217, v[114:115], off offset:1280
	global_load_dword v218, v[114:115], off offset:1536
	global_load_dword v219, v[114:115], off offset:1792
	v_lshl_add_u64 v[250:251], s[100:101], 0, v[78:79]
	global_load_dwordx2 v[112:113], v[126:127], off
	global_load_dwordx2 v[114:115], v[126:127], off offset:512
	global_load_dwordx2 v[116:117], v[126:127], off offset:1024
	global_load_dwordx2 v[118:119], v[126:127], off offset:1536
	global_load_dwordx2 v[120:121], v[126:127], off offset:2048
	global_load_dwordx2 v[122:123], v[126:127], off offset:2560
	global_load_dwordx2 v[124:125], v[126:127], off offset:3072
	s_nop 0
	global_load_dwordx2 v[126:127], v[126:127], off offset:3584
	s_nop 0
	global_load_dword v220, v[250:251], off
	global_load_dword v221, v[250:251], off offset:256
	global_load_dword v222, v[250:251], off offset:512
	global_load_dword v223, v[250:251], off offset:768
	global_load_dword v224, v[250:251], off offset:1024
	global_load_dword v225, v[250:251], off offset:1280
	global_load_dword v226, v[250:251], off offset:1536
	global_load_dword v227, v[250:251], off offset:1792
.Lpf_skip_1:
	v_lshlrev_b32_e32 v90, 16, v88
	v_and_b32_e32 v91, 0xffff0000, v88
	v_sub_f32_e32 v90, v86, v90
	v_sub_f32_e32 v91, v87, v91
	v_cvt_pk_bf16_f32 v89, v84, v85
	v_cvt_pk_bf16_f32 v90, v90, v91
	v_lshlrev_b32_e32 v128, 4, v128
	v_lshlrev_b32_e32 v91, 16, v89
	v_sub_f32_e32 v91, v84, v91
	v_and_b32_e32 v129, 0xffff0000, v89
	v_add3_u32 v128, s46, v128, v228
	v_sub_f32_e32 v129, v85, v129
	v_cvt_pk_bf16_f32 v91, v91, v129
	ds_write_b64 v128, v[88:89]
	v_add_u32_e32 v88, 0x10000, v128
	ds_write_b64 v88, v[90:91]
	v_mov_b32_e32 v90, 0
	v_cvt_pk_fp8_f32 v90, v154, v155
	v_mov_b32_e32 v91, 0
	v_cvt_pk_fp8_f32 v91, v174, v175
	v_lshl_add_u64 v[88:89], s[6:7], 0, v[78:79]
	v_cvt_pk_fp8_f32 v90, v152, v153 op_sel:[0,0,1]
	v_mov_b32_e32 v128, 0
	v_cvt_pk_fp8_f32 v91, v170, v171 op_sel:[0,0,1]
	v_cvt_pk_fp8_f32 v128, v186, v187
	global_store_dword v[88:89], v90, off
	v_lshl_add_u64 v[88:89], s[6:7], 0, v[76:77]
	v_mov_b32_e32 v90, 0
	global_store_dword v[88:89], v91, off
	v_cvt_pk_fp8_f32 v90, v158, v159
	v_mov_b32_e32 v91, 0
	v_cvt_pk_fp8_f32 v91, v178, v179
	v_cvt_pk_fp8_f32 v128, v184, v185 op_sel:[0,0,1]
	v_cvt_pk_fp8_f32 v90, v156, v157 op_sel:[0,0,1]
	v_lshl_add_u64 v[88:89], s[6:7], 0, v[74:75]
	v_cvt_pk_fp8_f32 v91, v176, v177 op_sel:[0,0,1]
	global_store_dword v[88:89], v128, off
	v_lshl_add_u64 v[88:89], s[6:7], 0, v[72:73]
	v_mov_b32_e32 v128, 0
	global_store_dword v[88:89], v90, off
	v_lshl_add_u64 v[88:89], s[6:7], 0, v[70:71]
	v_cvt_pk_fp8_f32 v128, v134, v135
	global_store_dword v[88:89], v91, off
	v_mov_b32_e32 v88, 0
	v_cvt_pk_fp8_f32 v88, v144, v145
	v_mov_b32_e32 v89, 0
	v_cvt_pk_fp8_f32 v89, v80, v81
	v_cvt_pk_fp8_f32 v128, v130, v131 op_sel:[0,0,1]
	v_cvt_pk_fp8_f32 v88, v242, v243 op_sel:[0,0,1]
	v_lshl_add_u64 v[80:81], s[6:7], 0, v[68:69]
	v_cvt_pk_fp8_f32 v89, v82, v83 op_sel:[0,0,1]
	global_store_dword v[80:81], v128, off
	v_lshl_add_u64 v[80:81], s[6:7], 0, v[66:67]
	global_store_dword v[80:81], v88, off
	v_lshl_add_u64 v[80:81], s[6:7], 0, v[64:65]
	global_store_dword v[80:81], v89, off
	v_mov_b32_e32 v80, 0
	v_mov_b32_e32 v81, 0
	v_cvt_pk_fp8_f32 v80, v146, v147
	v_cvt_pk_fp8_f32 v81, v164, v165
	s_add_i32 s6, s1, s18
	s_ashr_i32 s7, s6, 31
	s_lshl_b64 s[6:7], s[6:7], 11
	v_cvt_pk_fp8_f32 v80, v142, v143 op_sel:[0,0,1]
	v_cvt_pk_fp8_f32 v81, v162, v163 op_sel:[0,0,1]
	s_add_u32 s6, s41, s6
	s_addc_u32 s7, s42, s7
	v_lshl_add_u64 v[78:79], s[6:7], 0, v[78:79]
	v_lshl_add_u64 v[76:77], s[6:7], 0, v[76:77]
	v_mov_b32_e32 v82, 0
	global_store_dword v[78:79], v80, off
	global_store_dword v[76:77], v81, off
	v_mov_b32_e32 v76, 0
	v_mov_b32_e32 v77, 0
	v_cvt_pk_fp8_f32 v82, v182, v183
	v_cvt_pk_fp8_f32 v76, v150, v151
	v_cvt_pk_fp8_f32 v77, v172, v173
	v_lshl_add_u64 v[74:75], s[6:7], 0, v[74:75]
	v_cvt_pk_fp8_f32 v82, v180, v181 op_sel:[0,0,1]
	v_cvt_pk_fp8_f32 v76, v148, v149 op_sel:[0,0,1]
	v_cvt_pk_fp8_f32 v77, v168, v169 op_sel:[0,0,1]
	v_lshl_add_u64 v[72:73], s[6:7], 0, v[72:73]
	v_lshl_add_u64 v[70:71], s[6:7], 0, v[70:71]
	global_store_dword v[74:75], v82, off
	v_mov_b32_e32 v74, 0
	global_store_dword v[72:73], v76, off
	global_store_dword v[70:71], v77, off
	v_mov_b32_e32 v70, 0
	v_mov_b32_e32 v71, 0
	v_cvt_pk_fp8_f32 v74, v94, v95
	v_cvt_pk_fp8_f32 v70, v138, v139
	v_cvt_pk_fp8_f32 v71, v86, v87
	v_lshl_add_u64 v[68:69], s[6:7], 0, v[68:69]
	v_cvt_pk_fp8_f32 v74, v92, v93 op_sel:[0,0,1]
	v_cvt_pk_fp8_f32 v70, v136, v137 op_sel:[0,0,1]
	v_cvt_pk_fp8_f32 v71, v84, v85 op_sel:[0,0,1]
	v_lshl_add_u64 v[66:67], s[6:7], 0, v[66:67]
	v_lshl_add_u64 v[64:65], s[6:7], 0, v[64:65]
	global_store_dword v[68:69], v74, off
	global_store_dword v[66:67], v70, off
	global_store_dword v[64:65], v71, off
	s_waitcnt lgkmcnt(0)
	s_barrier
	ds_read_b128 v[64:67], v190
	ds_read_b128 v[68:71], v191
	s_waitcnt lgkmcnt(1)
	v_mfma_f32_16x16x32_bf16 v[72:75], v[0:3], v[64:67], 0
	v_mov_b32_e32 v128, v167
	v_mfma_f32_16x16x32_bf16 v[64:67], v[4:7], v[64:67], v[72:75]
	s_waitcnt lgkmcnt(0)
	v_mfma_f32_16x16x32_bf16 v[64:67], v[0:3], v[68:71], v[64:67]
	ds_read_b128 v[68:71], v192
	s_nop 2
	ds_read_b128 v[72:75], v193
	s_waitcnt lgkmcnt(1)
	v_mfma_f32_16x16x32_bf16 v[64:67], v[8:11], v[68:71], v[64:67]
	v_mfma_f32_16x16x32_bf16 v[64:67], v[12:15], v[68:71], v[64:67]
	s_waitcnt lgkmcnt(0)
	v_mfma_f32_16x16x32_bf16 v[64:67], v[8:11], v[72:75], v[64:67]
	ds_read_b128 v[68:71], v194
	ds_read_b128 v[72:75], v195
	s_waitcnt lgkmcnt(1)
	v_mfma_f32_16x16x32_bf16 v[64:67], v[16:19], v[68:71], v[64:67]
	v_mfma_f32_16x16x32_bf16 v[64:67], v[20:23], v[68:71], v[64:67]
	s_waitcnt lgkmcnt(0)
	v_mfma_f32_16x16x32_bf16 v[64:67], v[16:19], v[72:75], v[64:67]
	ds_read_b128 v[68:71], v196
	ds_read_b128 v[72:75], v197
	s_waitcnt lgkmcnt(1)
	v_mfma_f32_16x16x32_bf16 v[64:67], v[24:27], v[68:71], v[64:67]
	v_mfma_f32_16x16x32_bf16 v[64:67], v[28:31], v[68:71], v[64:67]
	s_waitcnt lgkmcnt(0)
	v_mfma_f32_16x16x32_bf16 v[64:67], v[24:27], v[72:75], v[64:67]
	ds_read_b128 v[68:71], v198
	ds_read_b128 v[72:75], v199
	s_waitcnt lgkmcnt(1)
	v_mfma_f32_16x16x32_bf16 v[64:67], v[32:35], v[68:71], v[64:67]
	v_mfma_f32_16x16x32_bf16 v[64:67], v[36:39], v[68:71], v[64:67]
	s_waitcnt lgkmcnt(0)
	v_mfma_f32_16x16x32_bf16 v[64:67], v[32:35], v[72:75], v[64:67]
	ds_read_b128 v[68:71], v200
	ds_read_b128 v[72:75], v201
	s_waitcnt lgkmcnt(1)
	v_mfma_f32_16x16x32_bf16 v[64:67], v[40:43], v[68:71], v[64:67]
	v_mfma_f32_16x16x32_bf16 v[64:67], v[44:47], v[68:71], v[64:67]
	s_waitcnt lgkmcnt(0)
	v_mfma_f32_16x16x32_bf16 v[64:67], v[40:43], v[72:75], v[64:67]
	ds_read_b128 v[68:71], v202
	ds_read_b128 v[72:75], v203
	s_waitcnt lgkmcnt(1)
	v_mfma_f32_16x16x32_bf16 v[64:67], v[48:51], v[68:71], v[64:67]
	v_mfma_f32_16x16x32_bf16 v[64:67], v[52:55], v[68:71], v[64:67]
	s_waitcnt lgkmcnt(0)
	v_mfma_f32_16x16x32_bf16 v[64:67], v[48:51], v[72:75], v[64:67]
	ds_read_b128 v[68:71], v204
	ds_read_b128 v[72:75], v205
	s_waitcnt lgkmcnt(1)
	v_mfma_f32_16x16x32_bf16 v[64:67], v[56:59], v[68:71], v[64:67]
	v_mfma_f32_16x16x32_bf16 v[64:67], v[60:63], v[68:71], v[64:67]
	s_waitcnt lgkmcnt(0)
	v_mfma_f32_16x16x32_bf16 v[64:67], v[56:59], v[72:75], v[64:67]
	s_nop 7
	ds_write_b128 v208, v[64:67]
	s_waitcnt lgkmcnt(0)
	s_barrier
	s_nop 0
	v_cmp_gt_i32_e32 vcc, s48, v128
	s_and_saveexec_b64 s[6:7], vcc
	s_cbranch_execz .LBB0_5172
	v_lshl_add_u32 v72, v128, 2, 0
	v_add_u32_e32 v70, 0x22000, v72
	ds_read2st64_b32 v[64:65], v70 offset1:4
	ds_read2st64_b32 v[66:67], v70 offset0:8 offset1:12
	ds_read2st64_b32 v[68:69], v70 offset0:16 offset1:20
	ds_read2st64_b32 v[70:71], v70 offset0:24 offset1:28
	s_waitcnt lgkmcnt(3)
	v_add_f32_e32 v64, 0, v64
	v_add_f32_e32 v64, v64, v65
	s_waitcnt lgkmcnt(2)
	v_add_f32_e32 v64, v64, v66
	v_add_f32_e32 v64, v64, v67
	s_waitcnt lgkmcnt(1)
	v_add_f32_e32 v64, v64, v68
	v_add_f32_e32 v64, v64, v69
	s_waitcnt lgkmcnt(0)
	v_add_f32_e32 v64, v64, v70
	v_add_f32_e32 v64, v64, v71
	v_add_u32_e32 v65, 0x21000, v72
	ds_write_b32 v65, v64
